# GEMM MFMA segments: removed the lgkmcnt(0) behind each barrier that repeats the one in front of it (40 sites)
# baseline (speedup 1.0000x reference)
.LBB0_243:
	ds_read_b128 v[74:77], v201
	ds_read_b128 v[78:81], v201 offset:1024
	ds_read_b128 v[82:85], v201 offset:2048
	ds_read_b128 v[86:89], v201 offset:3072
	ds_read_b128 v[164:167], v202
	ds_read_b128 v[168:171], v202 offset:1024
	ds_read_b128 v[172:175], v202 offset:2048
	ds_read_b128 v[176:179], v202 offset:3072
	s_add_u32 s26, s24, 0xfff80080
	s_addc_u32 s27, s25, -1
	s_cmp_eq_u32 s19, 28
	s_cselect_b32 s29, s21, s27
	s_cselect_b32 s28, s20, s26
	s_cselect_b32 s27, s23, s17
	s_cselect_b32 s26, s22, s7
	v_lshl_add_u64 v[228:229], s[24:25], 0, v[156:157]
	s_add_i32 m0, s41, 0xc000
	ds_read_b128 v[180:183], v203
	ds_read_b128 v[184:187], v203 offset:1024
	ds_read_b128 v[204:207], v203 offset:2048
	ds_read_b128 v[208:211], v203 offset:3072
	ds_read_b128 v[212:215], v203 offset:4096
	ds_read_b128 v[216:219], v203 offset:5120
	ds_read_b128 v[220:223], v203 offset:6144
	ds_read_b128 v[224:227], v203 offset:7168
	global_load_lds_dwordx4 v[228:229], off
	v_lshl_add_u64 v[228:229], s[24:25], 0, v[158:159]
	s_add_i32 m0, s41, 0xe000
	s_nop 0
	global_load_lds_dwordx4 v[228:229], off
	s_waitcnt vmcnt(8)
	s_waitcnt lgkmcnt(0)
	s_barrier
	s_setprio 1
	v_mfma_f32_16x16x32_bf16 v[142:145], v[74:77], v[180:183], v[142:145]
	v_mfma_f32_16x16x32_bf16 v[138:141], v[82:85], v[180:183], v[138:141]
	v_mfma_f32_16x16x32_bf16 v[126:129], v[74:77], v[204:207], v[126:129]
	v_mfma_f32_16x16x32_bf16 v[122:125], v[82:85], v[204:207], v[122:125]
	v_mfma_f32_16x16x32_bf16 v[110:113], v[74:77], v[212:215], v[110:113]
	v_mfma_f32_16x16x32_bf16 v[106:109], v[82:85], v[212:215], v[106:109]
	v_mfma_f32_16x16x32_bf16 v[94:97], v[74:77], v[220:223], v[94:97]
	v_mfma_f32_16x16x32_bf16 v[90:93], v[82:85], v[220:223], v[90:93]
	v_mfma_f32_16x16x32_bf16 v[142:145], v[78:81], v[184:187], v[142:145]
	v_mfma_f32_16x16x32_bf16 v[138:141], v[86:89], v[184:187], v[138:141]
	v_mfma_f32_16x16x32_bf16 v[126:129], v[78:81], v[208:211], v[126:129]
	v_mfma_f32_16x16x32_bf16 v[122:125], v[86:89], v[208:211], v[122:125]
	v_mfma_f32_16x16x32_bf16 v[110:113], v[78:81], v[216:219], v[110:113]
	v_mfma_f32_16x16x32_bf16 v[106:109], v[86:89], v[216:219], v[106:109]
	v_mfma_f32_16x16x32_bf16 v[94:97], v[78:81], v[224:227], v[94:97]
	v_mfma_f32_16x16x32_bf16 v[90:93], v[86:89], v[224:227], v[90:93]
	s_setprio 0
	s_setprio 1
	v_mfma_f32_16x16x32_bf16 v[134:137], v[164:167], v[180:183], v[134:137]
	v_mfma_f32_16x16x32_bf16 v[130:133], v[172:175], v[180:183], v[130:133]
	v_mfma_f32_16x16x32_bf16 v[118:121], v[164:167], v[204:207], v[118:121]
	v_mfma_f32_16x16x32_bf16 v[114:117], v[172:175], v[204:207], v[114:117]
	v_mfma_f32_16x16x32_bf16 v[102:105], v[164:167], v[212:215], v[102:105]
	v_mfma_f32_16x16x32_bf16 v[98:101], v[172:175], v[212:215], v[98:101]
	v_mfma_f32_16x16x32_bf16 v[70:73], v[164:167], v[220:223], v[70:73]
	v_mfma_f32_16x16x32_bf16 v[66:69], v[172:175], v[220:223], v[66:69]
	v_mfma_f32_16x16x32_bf16 v[134:137], v[168:171], v[184:187], v[134:137]
	v_mfma_f32_16x16x32_bf16 v[130:133], v[176:179], v[184:187], v[130:133]
	v_mfma_f32_16x16x32_bf16 v[118:121], v[168:171], v[208:211], v[118:121]
	v_mfma_f32_16x16x32_bf16 v[114:117], v[176:179], v[208:211], v[114:117]
	v_mfma_f32_16x16x32_bf16 v[102:105], v[168:171], v[216:219], v[102:105]
	v_mfma_f32_16x16x32_bf16 v[98:101], v[176:179], v[216:219], v[98:101]
	v_mfma_f32_16x16x32_bf16 v[70:73], v[168:171], v[224:227], v[70:73]
	v_mfma_f32_16x16x32_bf16 v[66:69], v[176:179], v[224:227], v[66:69]
	s_setprio 0
	s_barrier
	s_add_i32 s30, s53, s40
	v_lshl_add_u64 v[228:229], s[26:27], 0, v[148:149]
	s_mov_b32 m0, s30
	ds_read_b128 v[180:183], v203 offset:16384
	ds_read_b128 v[184:187], v203 offset:17408
	ds_read_b128 v[204:207], v203 offset:18432
	ds_read_b128 v[208:211], v203 offset:19456
	ds_read_b128 v[212:215], v203 offset:20480
	ds_read_b128 v[216:219], v203 offset:21504
	ds_read_b128 v[220:223], v203 offset:22528
	ds_read_b128 v[224:227], v203 offset:23552
	global_load_lds_dwordx4 v[228:229], off
	s_add_i32 m0, s30, 0x2000
	s_add_u32 s30, s26, 0x80000
	v_lshl_add_u64 v[230:231], s[26:27], 0, v[152:153]
	s_addc_u32 s31, s27, 0
	s_add_i32 s34, s54, s40
	global_load_lds_dwordx4 v[230:231], off
	v_lshl_add_u64 v[232:233], s[30:31], 0, v[148:149]
	s_mov_b32 m0, s34
	v_lshl_add_u64 v[234:235], s[28:29], 0, v[150:151]
	global_load_lds_dwordx4 v[232:233], off
	v_lshl_add_u64 v[232:233], s[30:31], 0, v[152:153]
	s_add_i32 m0, s34, 0x2000
	s_nop 0
	global_load_lds_dwordx4 v[232:233], off
	s_waitcnt vmcnt(6)
	s_waitcnt lgkmcnt(0)
	s_barrier
	s_setprio 1
	v_mfma_f32_16x16x32_bf16 v[62:65], v[74:77], v[180:183], v[62:65]
	v_mfma_f32_16x16x32_bf16 v[58:61], v[82:85], v[180:183], v[58:61]
	v_mfma_f32_16x16x32_bf16 v[46:49], v[74:77], v[204:207], v[46:49]
	v_mfma_f32_16x16x32_bf16 v[42:45], v[82:85], v[204:207], v[42:45]
	v_mfma_f32_16x16x32_bf16 v[30:33], v[74:77], v[212:215], v[30:33]
	v_mfma_f32_16x16x32_bf16 v[26:29], v[82:85], v[212:215], v[26:29]
	v_mfma_f32_16x16x32_bf16 v[14:17], v[74:77], v[220:223], v[14:17]
	v_mfma_f32_16x16x32_bf16 v[10:13], v[82:85], v[220:223], v[10:13]
	v_mfma_f32_16x16x32_bf16 v[62:65], v[78:81], v[184:187], v[62:65]
	v_lshl_add_u64 v[232:233], s[28:29], 0, v[146:147]
	s_mov_b32 m0, s41
	s_nop 0
	global_load_lds_dwordx4 v[232:233], off
	v_mfma_f32_16x16x32_bf16 v[58:61], v[86:89], v[184:187], v[58:61]
	v_mfma_f32_16x16x32_bf16 v[46:49], v[78:81], v[208:211], v[46:49]
	v_mfma_f32_16x16x32_bf16 v[42:45], v[86:89], v[208:211], v[42:45]
	v_mfma_f32_16x16x32_bf16 v[30:33], v[78:81], v[216:219], v[30:33]
	v_mfma_f32_16x16x32_bf16 v[26:29], v[86:89], v[216:219], v[26:29]
	v_mfma_f32_16x16x32_bf16 v[14:17], v[78:81], v[224:227], v[14:17]
	v_mfma_f32_16x16x32_bf16 v[10:13], v[86:89], v[224:227], v[10:13]
	s_setprio 0
	s_setprio 1
	v_mfma_f32_16x16x32_bf16 v[54:57], v[164:167], v[180:183], v[54:57]
	v_mfma_f32_16x16x32_bf16 v[50:53], v[172:175], v[180:183], v[50:53]
	v_mfma_f32_16x16x32_bf16 v[38:41], v[164:167], v[204:207], v[38:41]
	v_mfma_f32_16x16x32_bf16 v[34:37], v[172:175], v[204:207], v[34:37]
	v_mfma_f32_16x16x32_bf16 v[22:25], v[164:167], v[212:215], v[22:25]
	s_mov_b32 m0, s42
	s_nop 0
	global_load_lds_dwordx4 v[234:235], off
	v_mfma_f32_16x16x32_bf16 v[18:21], v[172:175], v[212:215], v[18:21]
	v_mfma_f32_16x16x32_bf16 v[6:9], v[164:167], v[220:223], v[6:9]
	v_mfma_f32_16x16x32_bf16 v[2:5], v[172:175], v[220:223], v[2:5]
	v_mfma_f32_16x16x32_bf16 v[54:57], v[168:171], v[184:187], v[54:57]
	v_mfma_f32_16x16x32_bf16 v[50:53], v[176:179], v[184:187], v[50:53]
	v_mfma_f32_16x16x32_bf16 v[38:41], v[168:171], v[208:211], v[38:41]
	v_mfma_f32_16x16x32_bf16 v[34:37], v[176:179], v[208:211], v[34:37]
	v_mfma_f32_16x16x32_bf16 v[22:25], v[168:171], v[216:219], v[22:25]
	v_mfma_f32_16x16x32_bf16 v[18:21], v[176:179], v[216:219], v[18:21]
	v_mfma_f32_16x16x32_bf16 v[6:9], v[168:171], v[224:227], v[6:9]
	v_mfma_f32_16x16x32_bf16 v[2:5], v[176:179], v[224:227], v[2:5]
	s_setprio 0
	s_barrier
	s_add_i32 s30, 0, 0x18000
	s_add_i32 s31, 0, 0x1c000
	v_add_u32_e32 v86, s30, v200
	v_add_u32_e32 v154, s31, v200
	ds_read_b128 v[74:77], v86
	ds_read_b128 v[78:81], v86 offset:1024
	ds_read_b128 v[82:85], v86 offset:2048
	ds_read_b128 v[86:89], v86 offset:3072
	ds_read_b128 v[164:167], v154
	ds_read_b128 v[168:171], v154 offset:1024
	ds_read_b128 v[172:175], v154 offset:2048
	ds_read_b128 v[176:179], v154 offset:3072
	s_add_u32 s28, s28, 0x80000
	s_addc_u32 s29, s29, 0
	s_mov_b32 m0, s43
	v_lshl_add_u64 v[236:237], s[28:29], 0, v[146:147]
	ds_read_b128 v[180:183], v203 offset:32768
	ds_read_b128 v[184:187], v203 offset:33792
	ds_read_b128 v[204:207], v203 offset:34816
	ds_read_b128 v[208:211], v203 offset:35840
	ds_read_b128 v[212:215], v203 offset:36864
	ds_read_b128 v[216:219], v203 offset:37888
	ds_read_b128 v[220:223], v203 offset:38912
	ds_read_b128 v[224:227], v203 offset:39936
	global_load_lds_dwordx4 v[236:237], off
	v_lshl_add_u64 v[236:237], s[28:29], 0, v[150:151]
	s_mov_b32 m0, s44
	s_nop 0
	global_load_lds_dwordx4 v[236:237], off
	s_waitcnt vmcnt(8)
	s_waitcnt lgkmcnt(0)
	s_barrier
	s_setprio 1
	v_mfma_f32_16x16x32_bf16 v[142:145], v[74:77], v[180:183], v[142:145]
	v_mfma_f32_16x16x32_bf16 v[138:141], v[82:85], v[180:183], v[138:141]
	v_mfma_f32_16x16x32_bf16 v[126:129], v[74:77], v[204:207], v[126:129]
	v_mfma_f32_16x16x32_bf16 v[122:125], v[82:85], v[204:207], v[122:125]
	v_mfma_f32_16x16x32_bf16 v[110:113], v[74:77], v[212:215], v[110:113]
	v_mfma_f32_16x16x32_bf16 v[106:109], v[82:85], v[212:215], v[106:109]
	v_mfma_f32_16x16x32_bf16 v[94:97], v[74:77], v[220:223], v[94:97]
	v_mfma_f32_16x16x32_bf16 v[90:93], v[82:85], v[220:223], v[90:93]
	v_mfma_f32_16x16x32_bf16 v[142:145], v[78:81], v[184:187], v[142:145]
	v_mfma_f32_16x16x32_bf16 v[138:141], v[86:89], v[184:187], v[138:141]
	v_mfma_f32_16x16x32_bf16 v[126:129], v[78:81], v[208:211], v[126:129]
	v_mfma_f32_16x16x32_bf16 v[122:125], v[86:89], v[208:211], v[122:125]
	v_mfma_f32_16x16x32_bf16 v[110:113], v[78:81], v[216:219], v[110:113]
	v_mfma_f32_16x16x32_bf16 v[106:109], v[86:89], v[216:219], v[106:109]
	v_mfma_f32_16x16x32_bf16 v[94:97], v[78:81], v[224:227], v[94:97]
	v_mfma_f32_16x16x32_bf16 v[90:93], v[86:89], v[224:227], v[90:93]
	s_setprio 0
	s_setprio 1
	v_mfma_f32_16x16x32_bf16 v[134:137], v[164:167], v[180:183], v[134:137]
	v_mfma_f32_16x16x32_bf16 v[130:133], v[172:175], v[180:183], v[130:133]
	v_mfma_f32_16x16x32_bf16 v[118:121], v[164:167], v[204:207], v[118:121]
	v_mfma_f32_16x16x32_bf16 v[114:117], v[172:175], v[204:207], v[114:117]
	v_mfma_f32_16x16x32_bf16 v[102:105], v[164:167], v[212:215], v[102:105]
	v_mfma_f32_16x16x32_bf16 v[98:101], v[172:175], v[212:215], v[98:101]
	v_mfma_f32_16x16x32_bf16 v[70:73], v[164:167], v[220:223], v[70:73]
	v_mfma_f32_16x16x32_bf16 v[66:69], v[172:175], v[220:223], v[66:69]
	v_mfma_f32_16x16x32_bf16 v[134:137], v[168:171], v[184:187], v[134:137]
	v_mfma_f32_16x16x32_bf16 v[130:133], v[176:179], v[184:187], v[130:133]
	v_mfma_f32_16x16x32_bf16 v[118:121], v[168:171], v[208:211], v[118:121]
	v_mfma_f32_16x16x32_bf16 v[114:117], v[176:179], v[208:211], v[114:117]
	v_mfma_f32_16x16x32_bf16 v[102:105], v[168:171], v[216:219], v[102:105]
	v_mfma_f32_16x16x32_bf16 v[98:101], v[176:179], v[216:219], v[98:101]
	v_mfma_f32_16x16x32_bf16 v[70:73], v[168:171], v[224:227], v[70:73]
	v_mfma_f32_16x16x32_bf16 v[66:69], v[176:179], v[224:227], v[66:69]
	s_setprio 0
	s_barrier
	s_add_i32 s28, s30, s40
	v_lshl_add_u64 v[228:229], v[228:229], 0, s[12:13]
	s_mov_b32 m0, s28
	ds_read_b128 v[180:183], v203 offset:49152
	ds_read_b128 v[184:187], v203 offset:50176
	ds_read_b128 v[204:207], v203 offset:51200
	ds_read_b128 v[208:211], v203 offset:52224
	ds_read_b128 v[212:215], v203 offset:53248
	ds_read_b128 v[216:219], v203 offset:54272
	ds_read_b128 v[220:223], v203 offset:55296
	ds_read_b128 v[224:227], v203 offset:56320
	global_load_lds_dwordx4 v[228:229], off
	s_add_i32 m0, s28, 0x2000
	s_add_u32 s26, s26, 0x80080
	v_lshl_add_u64 v[228:229], v[230:231], 0, s[12:13]
	s_addc_u32 s27, s27, 0
	s_add_i32 s28, s31, s40
	global_load_lds_dwordx4 v[228:229], off
	v_lshl_add_u64 v[228:229], s[26:27], 0, v[148:149]
	s_mov_b32 m0, s28
	s_nop 0
	global_load_lds_dwordx4 v[228:229], off
	v_lshl_add_u64 v[228:229], s[26:27], 0, v[152:153]
	s_add_i32 m0, s28, 0x2000
	s_nop 0
	global_load_lds_dwordx4 v[228:229], off
	s_waitcnt vmcnt(6)
	s_waitcnt lgkmcnt(0)
	s_barrier
	s_setprio 1
	v_mfma_f32_16x16x32_bf16 v[62:65], v[74:77], v[180:183], v[62:65]
	v_mfma_f32_16x16x32_bf16 v[58:61], v[82:85], v[180:183], v[58:61]
	v_mfma_f32_16x16x32_bf16 v[46:49], v[74:77], v[204:207], v[46:49]
	v_mfma_f32_16x16x32_bf16 v[42:45], v[82:85], v[204:207], v[42:45]
	v_mfma_f32_16x16x32_bf16 v[30:33], v[74:77], v[212:215], v[30:33]
	v_mfma_f32_16x16x32_bf16 v[26:29], v[82:85], v[212:215], v[26:29]
	v_mfma_f32_16x16x32_bf16 v[14:17], v[74:77], v[220:223], v[14:17]
	v_mfma_f32_16x16x32_bf16 v[10:13], v[82:85], v[220:223], v[10:13]
	v_mfma_f32_16x16x32_bf16 v[62:65], v[78:81], v[184:187], v[62:65]
	v_lshl_add_u64 v[228:229], v[232:233], 0, s[12:13]
	s_mov_b32 m0, s46
	s_nop 0
	global_load_lds_dwordx4 v[228:229], off
	v_mfma_f32_16x16x32_bf16 v[58:61], v[86:89], v[184:187], v[58:61]
	v_mfma_f32_16x16x32_bf16 v[46:49], v[78:81], v[208:211], v[46:49]
	v_mfma_f32_16x16x32_bf16 v[42:45], v[86:89], v[208:211], v[42:45]
	v_mfma_f32_16x16x32_bf16 v[30:33], v[78:81], v[216:219], v[30:33]
	v_mfma_f32_16x16x32_bf16 v[26:29], v[86:89], v[216:219], v[26:29]
	v_mfma_f32_16x16x32_bf16 v[14:17], v[78:81], v[224:227], v[14:17]
	v_mfma_f32_16x16x32_bf16 v[10:13], v[86:89], v[224:227], v[10:13]
	s_setprio 0
	s_setprio 1
	v_mfma_f32_16x16x32_bf16 v[54:57], v[164:167], v[180:183], v[54:57]
	v_mfma_f32_16x16x32_bf16 v[50:53], v[172:175], v[180:183], v[50:53]
	v_mfma_f32_16x16x32_bf16 v[38:41], v[164:167], v[204:207], v[38:41]
	v_mfma_f32_16x16x32_bf16 v[34:37], v[172:175], v[204:207], v[34:37]
	v_mfma_f32_16x16x32_bf16 v[22:25], v[164:167], v[212:215], v[22:25]
	v_lshl_add_u64 v[228:229], v[234:235], 0, s[12:13]
	s_mov_b32 m0, s47
	s_nop 0
	global_load_lds_dwordx4 v[228:229], off
	v_mfma_f32_16x16x32_bf16 v[18:21], v[172:175], v[212:215], v[18:21]
	v_mfma_f32_16x16x32_bf16 v[6:9], v[164:167], v[220:223], v[6:9]
	v_mfma_f32_16x16x32_bf16 v[2:5], v[172:175], v[220:223], v[2:5]
	v_mfma_f32_16x16x32_bf16 v[54:57], v[168:171], v[184:187], v[54:57]
	v_mfma_f32_16x16x32_bf16 v[50:53], v[176:179], v[184:187], v[50:53]
	v_mfma_f32_16x16x32_bf16 v[38:41], v[168:171], v[208:211], v[38:41]
	v_mfma_f32_16x16x32_bf16 v[34:37], v[176:179], v[208:211], v[34:37]
	v_mfma_f32_16x16x32_bf16 v[22:25], v[168:171], v[216:219], v[22:25]
	v_mfma_f32_16x16x32_bf16 v[18:21], v[176:179], v[216:219], v[18:21]
	v_mfma_f32_16x16x32_bf16 v[6:9], v[168:171], v[224:227], v[6:9]
	v_mfma_f32_16x16x32_bf16 v[2:5], v[176:179], v[224:227], v[2:5]
	s_setprio 0
	s_barrier
	s_add_i32 s19, s19, 2
	s_add_u32 s24, s24, 0x100
	s_addc_u32 s25, s25, 0
	s_add_u32 s7, s7, 0x100
	s_addc_u32 s17, s17, 0
	s_cmp_gt_u32 s19, 29
	s_cbranch_scc0 .LBB0_243
	s_and_b64 vcc, exec, s[14:15]
	s_cbranch_vccz .LBB0_246
	s_barrier

.LBB0_373:
	ds_read_b128 v[170:173], v1
	ds_read_b128 v[174:177], v156
	ds_read_b128 v[178:181], v157
	ds_read_b128 v[182:185], v158
	ds_read_b128 v[186:189], v159
	ds_read_b128 v[190:193], v160
	ds_read_b128 v[194:197], v161
	ds_read_b128 v[198:201], v162
	s_add_u32 s36, s6, 0xfffc0080
	s_addc_u32 s37, s7, -1
	s_cmp_eq_u32 s29, 12
	s_cselect_b32 s39, s31, s37
	s_cselect_b32 s38, s30, s36
	s_cselect_b32 s37, s35, s27
	s_cselect_b32 s36, s34, s9
	v_lshl_add_u64 v[148:149], s[6:7], 0, v[140:141]
	s_add_i32 m0, s43, 0xc000
	ds_read_b128 v[202:205], v163
	ds_read_b128 v[210:213], v163 offset:1024
	ds_read_b128 v[206:209], v164
	ds_read_b128 v[214:217], v164 offset:1024
	ds_read_b128 v[218:221], v163 offset:4096
	ds_read_b128 v[226:229], v163 offset:5120
	ds_read_b128 v[222:225], v164 offset:4096
	ds_read_b128 v[230:233], v164 offset:5120
	global_load_lds_dwordx4 v[148:149], off
	v_lshl_add_u64 v[148:149], s[6:7], 0, v[142:143]
	s_add_i32 m0, s43, 0xe000
	s_nop 0
	global_load_lds_dwordx4 v[148:149], off
	s_waitcnt vmcnt(8)
	s_waitcnt lgkmcnt(0)
	s_barrier
	s_setprio 1
	v_mfma_scale_f32_32x32x64_f8f6f4 v[114:129], v[170:177], v[202:209], v[114:129], v165, v165 op_sel_hi:[0,0,0]
	v_mfma_scale_f32_32x32x64_f8f6f4 v[82:97], v[170:177], v[218:225], v[82:97], v165, v165 op_sel_hi:[0,0,0]
	v_mfma_scale_f32_32x32x64_f8f6f4 v[114:129], v[178:185], v[210:217], v[114:129], v165, v165 op_sel_hi:[0,0,0]
	v_mfma_scale_f32_32x32x64_f8f6f4 v[82:97], v[178:185], v[226:233], v[82:97], v165, v165 op_sel_hi:[0,0,0]
	s_setprio 0
	s_setprio 1
	v_mfma_scale_f32_32x32x64_f8f6f4 v[98:113], v[186:193], v[202:209], v[98:113], v165, v165 op_sel_hi:[0,0,0]
	v_mfma_scale_f32_32x32x64_f8f6f4 v[66:81], v[186:193], v[218:225], v[66:81], v165, v165 op_sel_hi:[0,0,0]
	v_mfma_scale_f32_32x32x64_f8f6f4 v[98:113], v[194:201], v[210:217], v[98:113], v165, v165 op_sel_hi:[0,0,0]
	v_mfma_scale_f32_32x32x64_f8f6f4 v[66:81], v[194:201], v[226:233], v[66:81], v165, v165 op_sel_hi:[0,0,0]
	s_setprio 0
	s_barrier
	s_add_i32 s55, s51, s42
	v_lshl_add_u64 v[148:149], s[36:37], 0, v[132:133]
	s_mov_b32 m0, s55
	ds_read_b128 v[202:205], v163 offset:16384
	ds_read_b128 v[210:213], v163 offset:17408
	ds_read_b128 v[206:209], v164 offset:16384
	ds_read_b128 v[214:217], v164 offset:17408
	ds_read_b128 v[218:221], v163 offset:20480
	ds_read_b128 v[226:229], v163 offset:21504
	ds_read_b128 v[222:225], v164 offset:20480
	ds_read_b128 v[230:233], v164 offset:21504
	global_load_lds_dwordx4 v[148:149], off
	s_add_i32 m0, s55, 0x2000
	s_add_u32 s56, s36, 0x40000
	v_lshl_add_u64 v[150:151], s[36:37], 0, v[136:137]
	s_addc_u32 s57, s37, 0
	s_add_i32 s55, s52, s42
	global_load_lds_dwordx4 v[150:151], off
	v_lshl_add_u64 v[152:153], s[56:57], 0, v[132:133]
	s_mov_b32 m0, s55
	v_lshl_add_u64 v[234:235], s[38:39], 0, v[134:135]
	global_load_lds_dwordx4 v[152:153], off
	v_lshl_add_u64 v[152:153], s[56:57], 0, v[136:137]
	s_add_i32 m0, s55, 0x2000
	s_nop 0
	global_load_lds_dwordx4 v[152:153], off
	s_waitcnt vmcnt(6)
	s_waitcnt lgkmcnt(0)
	s_barrier
	s_setprio 1
	v_mfma_scale_f32_32x32x64_f8f6f4 v[50:65], v[170:177], v[202:209], v[50:65], v165, v165 op_sel_hi:[0,0,0]
	v_mfma_scale_f32_32x32x64_f8f6f4 v[18:33], v[170:177], v[218:225], v[18:33], v165, v165 op_sel_hi:[0,0,0]
	v_mfma_scale_f32_32x32x64_f8f6f4 v[50:65], v[178:185], v[210:217], v[50:65], v165, v165 op_sel_hi:[0,0,0]
	v_lshl_add_u64 v[152:153], s[38:39], 0, v[130:131]
	s_mov_b32 m0, s43
	s_nop 0
	global_load_lds_dwordx4 v[152:153], off
	v_mfma_scale_f32_32x32x64_f8f6f4 v[18:33], v[178:185], v[226:233], v[18:33], v165, v165 op_sel_hi:[0,0,0]
	s_setprio 0
	s_setprio 1
	v_mfma_scale_f32_32x32x64_f8f6f4 v[34:49], v[186:193], v[202:209], v[34:49], v165, v165 op_sel_hi:[0,0,0]
	v_mfma_scale_f32_32x32x64_f8f6f4 v[2:17], v[186:193], v[218:225], v[2:17], v165, v165 op_sel_hi:[0,0,0]
	s_mov_b32 m0, s44
	s_nop 0
	global_load_lds_dwordx4 v[234:235], off
	v_mfma_scale_f32_32x32x64_f8f6f4 v[34:49], v[194:201], v[210:217], v[34:49], v165, v165 op_sel_hi:[0,0,0]
	v_mfma_scale_f32_32x32x64_f8f6f4 v[2:17], v[194:201], v[226:233], v[2:17], v165, v165 op_sel_hi:[0,0,0]
	s_setprio 0
	s_barrier
	s_add_i32 s55, 0, 0x18000
	v_add_u32_e32 v138, s55, v154
	v_add_u32_e32 v174, s55, v155
	s_add_i32 s56, 0, 0x1c000
	ds_read_b128 v[170:173], v138
	ds_read_b128 v[174:177], v174
	ds_read_b128 v[178:181], v166
	ds_read_b128 v[182:185], v167
	v_add_u32_e32 v138, s56, v154
	v_add_u32_e32 v190, s56, v155
	ds_read_b128 v[186:189], v138
	ds_read_b128 v[190:193], v190
	ds_read_b128 v[194:197], v168
	ds_read_b128 v[198:201], v169
	s_add_u32 s38, s38, 0x40000
	s_addc_u32 s39, s39, 0
	s_mov_b32 m0, s45
	v_lshl_add_u64 v[236:237], s[38:39], 0, v[130:131]
	ds_read_b128 v[202:205], v163 offset:32768
	ds_read_b128 v[210:213], v163 offset:33792
	ds_read_b128 v[206:209], v164 offset:32768
	ds_read_b128 v[214:217], v164 offset:33792
	ds_read_b128 v[218:221], v163 offset:36864
	ds_read_b128 v[226:229], v163 offset:37888
	ds_read_b128 v[222:225], v164 offset:36864
	ds_read_b128 v[230:233], v164 offset:37888
	global_load_lds_dwordx4 v[236:237], off
	v_lshl_add_u64 v[236:237], s[38:39], 0, v[134:135]
	s_mov_b32 m0, s46
	s_nop 0
	global_load_lds_dwordx4 v[236:237], off
	s_waitcnt vmcnt(8)
	s_waitcnt lgkmcnt(0)
	s_barrier
	s_setprio 1
	v_mfma_scale_f32_32x32x64_f8f6f4 v[114:129], v[170:177], v[202:209], v[114:129], v165, v165 op_sel_hi:[0,0,0]
	v_mfma_scale_f32_32x32x64_f8f6f4 v[82:97], v[170:177], v[218:225], v[82:97], v165, v165 op_sel_hi:[0,0,0]
	v_mfma_scale_f32_32x32x64_f8f6f4 v[114:129], v[178:185], v[210:217], v[114:129], v165, v165 op_sel_hi:[0,0,0]
	v_mfma_scale_f32_32x32x64_f8f6f4 v[82:97], v[178:185], v[226:233], v[82:97], v165, v165 op_sel_hi:[0,0,0]
	s_setprio 0
	s_setprio 1
	v_mfma_scale_f32_32x32x64_f8f6f4 v[98:113], v[186:193], v[202:209], v[98:113], v165, v165 op_sel_hi:[0,0,0]
	v_mfma_scale_f32_32x32x64_f8f6f4 v[66:81], v[186:193], v[218:225], v[66:81], v165, v165 op_sel_hi:[0,0,0]
	v_mfma_scale_f32_32x32x64_f8f6f4 v[98:113], v[194:201], v[210:217], v[98:113], v165, v165 op_sel_hi:[0,0,0]
	v_mfma_scale_f32_32x32x64_f8f6f4 v[66:81], v[194:201], v[226:233], v[66:81], v165, v165 op_sel_hi:[0,0,0]
	s_setprio 0
	s_barrier
	s_add_i32 s38, s55, s42
	v_lshl_add_u64 v[148:149], v[148:149], 0, s[16:17]
	s_mov_b32 m0, s38
	ds_read_b128 v[202:205], v163 offset:49152
	ds_read_b128 v[210:213], v163 offset:50176
	ds_read_b128 v[206:209], v164 offset:49152
	ds_read_b128 v[214:217], v164 offset:50176
	ds_read_b128 v[218:221], v163 offset:53248
	ds_read_b128 v[226:229], v163 offset:54272
	ds_read_b128 v[222:225], v164 offset:53248
	ds_read_b128 v[230:233], v164 offset:54272
	global_load_lds_dwordx4 v[148:149], off
	s_add_i32 m0, s38, 0x2000
	s_add_u32 s36, s36, 0x40080
	v_lshl_add_u64 v[148:149], v[150:151], 0, s[16:17]
	s_addc_u32 s37, s37, 0
	s_add_i32 s38, s56, s42
	global_load_lds_dwordx4 v[148:149], off
	v_lshl_add_u64 v[148:149], s[36:37], 0, v[132:133]
	s_mov_b32 m0, s38
	s_nop 0
	global_load_lds_dwordx4 v[148:149], off
	v_lshl_add_u64 v[148:149], s[36:37], 0, v[136:137]
	s_add_i32 m0, s38, 0x2000
	s_nop 0
	global_load_lds_dwordx4 v[148:149], off
	s_waitcnt vmcnt(6)
	s_waitcnt lgkmcnt(0)
	s_barrier
	s_setprio 1
	v_mfma_scale_f32_32x32x64_f8f6f4 v[50:65], v[170:177], v[202:209], v[50:65], v165, v165 op_sel_hi:[0,0,0]
	v_mfma_scale_f32_32x32x64_f8f6f4 v[18:33], v[170:177], v[218:225], v[18:33], v165, v165 op_sel_hi:[0,0,0]
	v_mfma_scale_f32_32x32x64_f8f6f4 v[50:65], v[178:185], v[210:217], v[50:65], v165, v165 op_sel_hi:[0,0,0]
	v_lshl_add_u64 v[148:149], v[152:153], 0, s[16:17]
	s_mov_b32 m0, s47
	s_nop 0
	global_load_lds_dwordx4 v[148:149], off
	v_mfma_scale_f32_32x32x64_f8f6f4 v[18:33], v[178:185], v[226:233], v[18:33], v165, v165 op_sel_hi:[0,0,0]
	s_setprio 0
	s_setprio 1
	v_mfma_scale_f32_32x32x64_f8f6f4 v[34:49], v[186:193], v[202:209], v[34:49], v165, v165 op_sel_hi:[0,0,0]
	v_mfma_scale_f32_32x32x64_f8f6f4 v[2:17], v[186:193], v[218:225], v[2:17], v165, v165 op_sel_hi:[0,0,0]
	v_lshl_add_u64 v[148:149], v[234:235], 0, s[16:17]
	s_mov_b32 m0, s48
	s_nop 0
	global_load_lds_dwordx4 v[148:149], off
	v_mfma_scale_f32_32x32x64_f8f6f4 v[34:49], v[194:201], v[210:217], v[34:49], v165, v165 op_sel_hi:[0,0,0]
	v_mfma_scale_f32_32x32x64_f8f6f4 v[2:17], v[194:201], v[226:233], v[2:17], v165, v165 op_sel_hi:[0,0,0]
	s_setprio 0
	s_barrier
	s_add_i32 s29, s29, 2
	s_add_u32 s6, s6, 0x100
	s_addc_u32 s7, s7, 0
	s_add_u32 s9, s9, 0x100
	s_addc_u32 s27, s27, 0
	s_cmp_gt_u32 s29, 13
	s_cbranch_scc0 .LBB0_373
	s_and_b64 vcc, exec, s[18:19]
	s_cbranch_vccz .LBB0_376
	s_barrier

.LBB0_407:
	ds_read_b128 v[150:153], v147
	ds_read_b128 v[154:157], v147 offset:1024
	ds_read_b128 v[158:161], v147 offset:2048
	ds_read_b128 v[162:165], v147 offset:3072
	ds_read_b128 v[166:169], v148
	ds_read_b128 v[170:173], v148 offset:1024
	ds_read_b128 v[174:177], v148 offset:2048
	ds_read_b128 v[178:181], v148 offset:3072
	s_add_u32 s40, s38, 0xfff80080
	s_addc_u32 s41, s39, -1
	s_cmp_eq_u32 s68, 28
	s_cselect_b32 s43, s29, s41
	s_cselect_b32 s42, s28, s40
	s_cselect_b32 s41, s31, s37
	s_cselect_b32 s40, s30, s27
	v_lshl_add_u64 v[214:215], s[38:39], 0, v[140:141]
	s_add_i32 m0, s47, 0xc000
	ds_read_b128 v[182:185], v149
	ds_read_b128 v[186:189], v149 offset:1024
	ds_read_b128 v[190:193], v149 offset:2048
	ds_read_b128 v[194:197], v149 offset:3072
	ds_read_b128 v[198:201], v149 offset:4096
	ds_read_b128 v[202:205], v149 offset:5120
	ds_read_b128 v[206:209], v149 offset:6144
	ds_read_b128 v[210:213], v149 offset:7168
	global_load_lds_dwordx4 v[214:215], off
	v_lshl_add_u64 v[214:215], s[38:39], 0, v[142:143]
	s_add_i32 m0, s47, 0xe000
	s_nop 0
	global_load_lds_dwordx4 v[214:215], off
	s_waitcnt vmcnt(8)
	s_waitcnt lgkmcnt(0)
	s_barrier
	s_setprio 1
	v_mfma_f32_16x16x32_bf16 v[126:129], v[150:153], v[182:185], v[126:129]
	v_mfma_f32_16x16x32_bf16 v[122:125], v[158:161], v[182:185], v[122:125]
	v_mfma_f32_16x16x32_bf16 v[118:121], v[150:153], v[190:193], v[118:121]
	v_mfma_f32_16x16x32_bf16 v[114:117], v[158:161], v[190:193], v[114:117]
	v_mfma_f32_16x16x32_bf16 v[110:113], v[150:153], v[198:201], v[110:113]
	v_mfma_f32_16x16x32_bf16 v[102:105], v[158:161], v[198:201], v[102:105]
	v_mfma_f32_16x16x32_bf16 v[86:89], v[150:153], v[206:209], v[86:89]
	v_mfma_f32_16x16x32_bf16 v[74:77], v[158:161], v[206:209], v[74:77]
	v_mfma_f32_16x16x32_bf16 v[126:129], v[154:157], v[186:189], v[126:129]
	v_mfma_f32_16x16x32_bf16 v[122:125], v[162:165], v[186:189], v[122:125]
	v_mfma_f32_16x16x32_bf16 v[118:121], v[154:157], v[194:197], v[118:121]
	v_mfma_f32_16x16x32_bf16 v[114:117], v[162:165], v[194:197], v[114:117]
	v_mfma_f32_16x16x32_bf16 v[110:113], v[154:157], v[202:205], v[110:113]
	v_mfma_f32_16x16x32_bf16 v[102:105], v[162:165], v[202:205], v[102:105]
	v_mfma_f32_16x16x32_bf16 v[86:89], v[154:157], v[210:213], v[86:89]
	v_mfma_f32_16x16x32_bf16 v[74:77], v[162:165], v[210:213], v[74:77]
	s_setprio 0
	s_setprio 1
	v_mfma_f32_16x16x32_bf16 v[106:109], v[166:169], v[182:185], v[106:109]
	v_mfma_f32_16x16x32_bf16 v[98:101], v[174:177], v[182:185], v[98:101]
	v_mfma_f32_16x16x32_bf16 v[94:97], v[166:169], v[190:193], v[94:97]
	v_mfma_f32_16x16x32_bf16 v[90:93], v[174:177], v[190:193], v[90:93]
	v_mfma_f32_16x16x32_bf16 v[82:85], v[166:169], v[198:201], v[82:85]
	v_mfma_f32_16x16x32_bf16 v[78:81], v[174:177], v[198:201], v[78:81]
	v_mfma_f32_16x16x32_bf16 v[70:73], v[166:169], v[206:209], v[70:73]
	v_mfma_f32_16x16x32_bf16 v[66:69], v[174:177], v[206:209], v[66:69]
	v_mfma_f32_16x16x32_bf16 v[106:109], v[170:173], v[186:189], v[106:109]
	v_mfma_f32_16x16x32_bf16 v[98:101], v[178:181], v[186:189], v[98:101]
	v_mfma_f32_16x16x32_bf16 v[94:97], v[170:173], v[194:197], v[94:97]
	v_mfma_f32_16x16x32_bf16 v[90:93], v[178:181], v[194:197], v[90:93]
	v_mfma_f32_16x16x32_bf16 v[82:85], v[170:173], v[202:205], v[82:85]
	v_mfma_f32_16x16x32_bf16 v[78:81], v[178:181], v[202:205], v[78:81]
	v_mfma_f32_16x16x32_bf16 v[70:73], v[170:173], v[210:213], v[70:73]
	v_mfma_f32_16x16x32_bf16 v[66:69], v[178:181], v[210:213], v[66:69]
	s_setprio 0
	s_barrier
	s_add_i32 s69, s57, s3
	v_lshl_add_u64 v[214:215], s[40:41], 0, v[134:135]
	s_mov_b32 m0, s69
	ds_read_b128 v[182:185], v149 offset:16384
	ds_read_b128 v[186:189], v149 offset:17408
	ds_read_b128 v[190:193], v149 offset:18432
	ds_read_b128 v[194:197], v149 offset:19456
	ds_read_b128 v[198:201], v149 offset:20480
	ds_read_b128 v[202:205], v149 offset:21504
	ds_read_b128 v[206:209], v149 offset:22528
	ds_read_b128 v[210:213], v149 offset:23552
	global_load_lds_dwordx4 v[214:215], off
	s_add_i32 m0, s69, 0x2000
	s_add_u32 s70, s40, 0x80000
	v_lshl_add_u64 v[216:217], s[40:41], 0, v[130:131]
	s_addc_u32 s71, s41, 0
	s_add_i32 s69, s58, s3
	global_load_lds_dwordx4 v[216:217], off
	v_lshl_add_u64 v[218:219], s[70:71], 0, v[134:135]
	s_mov_b32 m0, s69
	v_lshl_add_u64 v[220:221], s[42:43], 0, v[132:133]
	global_load_lds_dwordx4 v[218:219], off
	v_lshl_add_u64 v[218:219], s[70:71], 0, v[130:131]
	s_add_i32 m0, s69, 0x2000
	s_nop 0
	global_load_lds_dwordx4 v[218:219], off
	s_waitcnt vmcnt(6)
	s_waitcnt lgkmcnt(0)
	s_barrier
	s_setprio 1
	v_mfma_f32_16x16x32_bf16 v[62:65], v[150:153], v[182:185], v[62:65]
	v_mfma_f32_16x16x32_bf16 v[58:61], v[158:161], v[182:185], v[58:61]
	v_mfma_f32_16x16x32_bf16 v[54:57], v[150:153], v[190:193], v[54:57]
	v_mfma_f32_16x16x32_bf16 v[46:49], v[158:161], v[190:193], v[46:49]
	v_mfma_f32_16x16x32_bf16 v[38:41], v[150:153], v[198:201], v[38:41]
	v_mfma_f32_16x16x32_bf16 v[30:33], v[158:161], v[198:201], v[30:33]
	v_mfma_f32_16x16x32_bf16 v[22:25], v[150:153], v[206:209], v[22:25]
	v_mfma_f32_16x16x32_bf16 v[14:17], v[158:161], v[206:209], v[14:17]
	v_mfma_f32_16x16x32_bf16 v[62:65], v[154:157], v[186:189], v[62:65]
	v_lshl_add_u64 v[218:219], s[42:43], 0, v[136:137]
	s_mov_b32 m0, s47
	s_nop 0
	global_load_lds_dwordx4 v[218:219], off
	v_mfma_f32_16x16x32_bf16 v[58:61], v[162:165], v[186:189], v[58:61]
	v_mfma_f32_16x16x32_bf16 v[54:57], v[154:157], v[194:197], v[54:57]
	v_mfma_f32_16x16x32_bf16 v[46:49], v[162:165], v[194:197], v[46:49]
	v_mfma_f32_16x16x32_bf16 v[38:41], v[154:157], v[202:205], v[38:41]
	v_mfma_f32_16x16x32_bf16 v[30:33], v[162:165], v[202:205], v[30:33]
	v_mfma_f32_16x16x32_bf16 v[22:25], v[154:157], v[210:213], v[22:25]
	v_mfma_f32_16x16x32_bf16 v[14:17], v[162:165], v[210:213], v[14:17]
	s_setprio 0
	s_setprio 1
	v_mfma_f32_16x16x32_bf16 v[50:53], v[166:169], v[182:185], v[50:53]
	v_mfma_f32_16x16x32_bf16 v[42:45], v[174:177], v[182:185], v[42:45]
	v_mfma_f32_16x16x32_bf16 v[34:37], v[166:169], v[190:193], v[34:37]
	v_mfma_f32_16x16x32_bf16 v[26:29], v[174:177], v[190:193], v[26:29]
	v_mfma_f32_16x16x32_bf16 v[18:21], v[166:169], v[198:201], v[18:21]
	s_mov_b32 m0, s48
	s_nop 0
	global_load_lds_dwordx4 v[220:221], off
	v_mfma_f32_16x16x32_bf16 v[10:13], v[174:177], v[198:201], v[10:13]
	v_mfma_f32_16x16x32_bf16 v[6:9], v[166:169], v[206:209], v[6:9]
	v_mfma_f32_16x16x32_bf16 v[2:5], v[174:177], v[206:209], v[2:5]
	v_mfma_f32_16x16x32_bf16 v[50:53], v[170:173], v[186:189], v[50:53]
	v_mfma_f32_16x16x32_bf16 v[42:45], v[178:181], v[186:189], v[42:45]
	v_mfma_f32_16x16x32_bf16 v[34:37], v[170:173], v[194:197], v[34:37]
	v_mfma_f32_16x16x32_bf16 v[26:29], v[178:181], v[194:197], v[26:29]
	v_mfma_f32_16x16x32_bf16 v[18:21], v[170:173], v[202:205], v[18:21]
	v_mfma_f32_16x16x32_bf16 v[10:13], v[178:181], v[202:205], v[10:13]
	v_mfma_f32_16x16x32_bf16 v[6:9], v[170:173], v[210:213], v[6:9]
	v_mfma_f32_16x16x32_bf16 v[2:5], v[178:181], v[210:213], v[2:5]
	s_setprio 0
	s_barrier
	s_add_i32 s69, 0, 0x18000
	v_add_u32_e32 v138, s69, v145
	s_add_i32 s70, 0, 0x1c000
	ds_read_b128 v[150:153], v138
	ds_read_b128 v[154:157], v138 offset:1024
	ds_read_b128 v[158:161], v138 offset:2048
	ds_read_b128 v[162:165], v138 offset:3072
	v_add_u32_e32 v138, s70, v145
	ds_read_b128 v[166:169], v138
	ds_read_b128 v[170:173], v138 offset:1024
	ds_read_b128 v[174:177], v138 offset:2048
	ds_read_b128 v[178:181], v138 offset:3072
	s_add_u32 s42, s42, 0x80000
	s_addc_u32 s43, s43, 0
	s_mov_b32 m0, s49
	v_lshl_add_u64 v[222:223], s[42:43], 0, v[136:137]
	ds_read_b128 v[182:185], v149 offset:32768
	ds_read_b128 v[186:189], v149 offset:33792
	ds_read_b128 v[190:193], v149 offset:34816
	ds_read_b128 v[194:197], v149 offset:35840
	ds_read_b128 v[198:201], v149 offset:36864
	ds_read_b128 v[202:205], v149 offset:37888
	ds_read_b128 v[206:209], v149 offset:38912
	ds_read_b128 v[210:213], v149 offset:39936
	global_load_lds_dwordx4 v[222:223], off
	v_lshl_add_u64 v[222:223], s[42:43], 0, v[132:133]
	s_mov_b32 m0, s50
	s_nop 0
	global_load_lds_dwordx4 v[222:223], off
	s_waitcnt vmcnt(8)
	s_waitcnt lgkmcnt(0)
	s_barrier
	s_setprio 1
	v_mfma_f32_16x16x32_bf16 v[126:129], v[150:153], v[182:185], v[126:129]
	v_mfma_f32_16x16x32_bf16 v[122:125], v[158:161], v[182:185], v[122:125]
	v_mfma_f32_16x16x32_bf16 v[118:121], v[150:153], v[190:193], v[118:121]
	v_mfma_f32_16x16x32_bf16 v[114:117], v[158:161], v[190:193], v[114:117]
	v_mfma_f32_16x16x32_bf16 v[110:113], v[150:153], v[198:201], v[110:113]
	v_mfma_f32_16x16x32_bf16 v[102:105], v[158:161], v[198:201], v[102:105]
	v_mfma_f32_16x16x32_bf16 v[86:89], v[150:153], v[206:209], v[86:89]
	v_mfma_f32_16x16x32_bf16 v[74:77], v[158:161], v[206:209], v[74:77]
	v_mfma_f32_16x16x32_bf16 v[126:129], v[154:157], v[186:189], v[126:129]
	v_mfma_f32_16x16x32_bf16 v[122:125], v[162:165], v[186:189], v[122:125]
	v_mfma_f32_16x16x32_bf16 v[118:121], v[154:157], v[194:197], v[118:121]
	v_mfma_f32_16x16x32_bf16 v[114:117], v[162:165], v[194:197], v[114:117]
	v_mfma_f32_16x16x32_bf16 v[110:113], v[154:157], v[202:205], v[110:113]
	v_mfma_f32_16x16x32_bf16 v[102:105], v[162:165], v[202:205], v[102:105]
	v_mfma_f32_16x16x32_bf16 v[86:89], v[154:157], v[210:213], v[86:89]
	v_mfma_f32_16x16x32_bf16 v[74:77], v[162:165], v[210:213], v[74:77]
	s_setprio 0
	s_setprio 1
	v_mfma_f32_16x16x32_bf16 v[106:109], v[166:169], v[182:185], v[106:109]
	v_mfma_f32_16x16x32_bf16 v[98:101], v[174:177], v[182:185], v[98:101]
	v_mfma_f32_16x16x32_bf16 v[94:97], v[166:169], v[190:193], v[94:97]
	v_mfma_f32_16x16x32_bf16 v[90:93], v[174:177], v[190:193], v[90:93]
	v_mfma_f32_16x16x32_bf16 v[82:85], v[166:169], v[198:201], v[82:85]
	v_mfma_f32_16x16x32_bf16 v[78:81], v[174:177], v[198:201], v[78:81]
	v_mfma_f32_16x16x32_bf16 v[70:73], v[166:169], v[206:209], v[70:73]
	v_mfma_f32_16x16x32_bf16 v[66:69], v[174:177], v[206:209], v[66:69]
	v_mfma_f32_16x16x32_bf16 v[106:109], v[170:173], v[186:189], v[106:109]
	v_mfma_f32_16x16x32_bf16 v[98:101], v[178:181], v[186:189], v[98:101]
	v_mfma_f32_16x16x32_bf16 v[94:97], v[170:173], v[194:197], v[94:97]
	v_mfma_f32_16x16x32_bf16 v[90:93], v[178:181], v[194:197], v[90:93]
	v_mfma_f32_16x16x32_bf16 v[82:85], v[170:173], v[202:205], v[82:85]
	v_mfma_f32_16x16x32_bf16 v[78:81], v[178:181], v[202:205], v[78:81]
	v_mfma_f32_16x16x32_bf16 v[70:73], v[170:173], v[210:213], v[70:73]
	v_mfma_f32_16x16x32_bf16 v[66:69], v[178:181], v[210:213], v[66:69]
	s_setprio 0
	s_barrier
	s_add_i32 s42, s69, s3
	v_lshl_add_u64 v[214:215], v[214:215], 0, s[16:17]
	s_mov_b32 m0, s42
	ds_read_b128 v[182:185], v149 offset:49152
	ds_read_b128 v[186:189], v149 offset:50176
	ds_read_b128 v[190:193], v149 offset:51200
	ds_read_b128 v[194:197], v149 offset:52224
	ds_read_b128 v[198:201], v149 offset:53248
	ds_read_b128 v[202:205], v149 offset:54272
	ds_read_b128 v[206:209], v149 offset:55296
	ds_read_b128 v[210:213], v149 offset:56320
	global_load_lds_dwordx4 v[214:215], off
	s_add_i32 m0, s42, 0x2000
	s_add_u32 s40, s40, 0x80080
	v_lshl_add_u64 v[214:215], v[216:217], 0, s[16:17]
	s_addc_u32 s41, s41, 0
	s_add_i32 s42, s70, s3
	global_load_lds_dwordx4 v[214:215], off
	v_lshl_add_u64 v[214:215], s[40:41], 0, v[134:135]
	s_mov_b32 m0, s42
	s_nop 0
	global_load_lds_dwordx4 v[214:215], off
	v_lshl_add_u64 v[214:215], s[40:41], 0, v[130:131]
	s_add_i32 m0, s42, 0x2000
	s_nop 0
	global_load_lds_dwordx4 v[214:215], off
	s_waitcnt vmcnt(6)
	s_waitcnt lgkmcnt(0)
	s_barrier
	s_setprio 1
	v_mfma_f32_16x16x32_bf16 v[62:65], v[150:153], v[182:185], v[62:65]
	v_mfma_f32_16x16x32_bf16 v[58:61], v[158:161], v[182:185], v[58:61]
	v_mfma_f32_16x16x32_bf16 v[54:57], v[150:153], v[190:193], v[54:57]
	v_mfma_f32_16x16x32_bf16 v[46:49], v[158:161], v[190:193], v[46:49]
	v_mfma_f32_16x16x32_bf16 v[38:41], v[150:153], v[198:201], v[38:41]
	v_mfma_f32_16x16x32_bf16 v[30:33], v[158:161], v[198:201], v[30:33]
	v_mfma_f32_16x16x32_bf16 v[22:25], v[150:153], v[206:209], v[22:25]
	v_mfma_f32_16x16x32_bf16 v[14:17], v[158:161], v[206:209], v[14:17]
	v_mfma_f32_16x16x32_bf16 v[62:65], v[154:157], v[186:189], v[62:65]
	v_lshl_add_u64 v[214:215], v[218:219], 0, s[16:17]
	s_mov_b32 m0, s55
	s_nop 0
	global_load_lds_dwordx4 v[214:215], off
	v_mfma_f32_16x16x32_bf16 v[58:61], v[162:165], v[186:189], v[58:61]
	v_mfma_f32_16x16x32_bf16 v[54:57], v[154:157], v[194:197], v[54:57]
	v_mfma_f32_16x16x32_bf16 v[46:49], v[162:165], v[194:197], v[46:49]
	v_mfma_f32_16x16x32_bf16 v[38:41], v[154:157], v[202:205], v[38:41]
	v_mfma_f32_16x16x32_bf16 v[30:33], v[162:165], v[202:205], v[30:33]
	v_mfma_f32_16x16x32_bf16 v[22:25], v[154:157], v[210:213], v[22:25]
	v_mfma_f32_16x16x32_bf16 v[14:17], v[162:165], v[210:213], v[14:17]
	s_setprio 0
	s_setprio 1
	v_mfma_f32_16x16x32_bf16 v[50:53], v[166:169], v[182:185], v[50:53]
	v_mfma_f32_16x16x32_bf16 v[42:45], v[174:177], v[182:185], v[42:45]
	v_mfma_f32_16x16x32_bf16 v[34:37], v[166:169], v[190:193], v[34:37]
	v_mfma_f32_16x16x32_bf16 v[26:29], v[174:177], v[190:193], v[26:29]
	v_mfma_f32_16x16x32_bf16 v[18:21], v[166:169], v[198:201], v[18:21]
	v_lshl_add_u64 v[214:215], v[220:221], 0, s[16:17]
	s_mov_b32 m0, s56
	s_nop 0
	global_load_lds_dwordx4 v[214:215], off
	v_mfma_f32_16x16x32_bf16 v[10:13], v[174:177], v[198:201], v[10:13]
	v_mfma_f32_16x16x32_bf16 v[6:9], v[166:169], v[206:209], v[6:9]
	v_mfma_f32_16x16x32_bf16 v[2:5], v[174:177], v[206:209], v[2:5]
	v_mfma_f32_16x16x32_bf16 v[50:53], v[170:173], v[186:189], v[50:53]
	v_mfma_f32_16x16x32_bf16 v[42:45], v[178:181], v[186:189], v[42:45]
	v_mfma_f32_16x16x32_bf16 v[34:37], v[170:173], v[194:197], v[34:37]
	v_mfma_f32_16x16x32_bf16 v[26:29], v[178:181], v[194:197], v[26:29]
	v_mfma_f32_16x16x32_bf16 v[18:21], v[170:173], v[202:205], v[18:21]
	v_mfma_f32_16x16x32_bf16 v[10:13], v[178:181], v[202:205], v[10:13]
	v_mfma_f32_16x16x32_bf16 v[6:9], v[170:173], v[210:213], v[6:9]
	v_mfma_f32_16x16x32_bf16 v[2:5], v[178:181], v[210:213], v[2:5]
	s_setprio 0
	s_barrier
	s_add_i32 s68, s68, 2
	s_add_u32 s38, s38, 0x100
	s_addc_u32 s39, s39, 0
	s_add_u32 s27, s27, 0x100
	s_addc_u32 s37, s37, 0
	s_cmp_gt_u32 s68, 29
	s_cbranch_scc0 .LBB0_407
	s_and_b64 vcc, exec, s[18:19]
	s_cbranch_vccz .LBB0_410
	s_barrier

.LBB0_769:
	ds_read_b128 v[130:133], v159
	ds_read_b128 v[134:137], v160
	ds_read_b128 v[174:177], v161
	ds_read_b128 v[178:181], v162
	ds_read_b128 v[182:185], v163
	ds_read_b128 v[186:189], v164
	ds_read_b128 v[190:193], v165
	ds_read_b128 v[194:197], v166
	s_add_u32 s44, s42, 0xfffc0080
	s_addc_u32 s45, s43, -1
	s_cmp_eq_u32 s41, 12
	s_cselect_b32 s47, s37, s45
	s_cselect_b32 s46, s36, s44
	s_cselect_b32 s45, s39, s35
	s_cselect_b32 s44, s38, s31
	v_lshl_add_u64 v[154:155], s[42:43], 0, v[146:147]
	s_add_i32 m0, s51, 0xc000
	ds_read_b128 v[198:201], v167
	ds_read_b128 v[206:209], v167 offset:1024
	ds_read_b128 v[202:205], v168
	ds_read_b128 v[210:213], v168 offset:1024
	ds_read_b128 v[214:217], v167 offset:4096
	ds_read_b128 v[222:225], v167 offset:5120
	ds_read_b128 v[218:221], v168 offset:4096
	ds_read_b128 v[226:229], v168 offset:5120
	global_load_lds_dwordx4 v[154:155], off
	v_lshl_add_u64 v[154:155], s[42:43], 0, v[148:149]
	s_add_i32 m0, s51, 0xe000
	s_nop 0
	global_load_lds_dwordx4 v[154:155], off
	s_waitcnt vmcnt(8)
	s_waitcnt lgkmcnt(0)
	s_barrier
	s_setprio 1
	v_mfma_scale_f32_32x32x64_f8f6f4 v[114:129], v[130:137], v[198:205], v[114:129], v169, v169 op_sel_hi:[0,0,0]
	v_mfma_scale_f32_32x32x64_f8f6f4 v[82:97], v[130:137], v[214:221], v[82:97], v169, v169 op_sel_hi:[0,0,0]
	v_mfma_scale_f32_32x32x64_f8f6f4 v[114:129], v[174:181], v[206:213], v[114:129], v169, v169 op_sel_hi:[0,0,0]
	v_mfma_scale_f32_32x32x64_f8f6f4 v[82:97], v[174:181], v[222:229], v[82:97], v169, v169 op_sel_hi:[0,0,0]
	s_setprio 0
	s_setprio 1
	v_mfma_scale_f32_32x32x64_f8f6f4 v[98:113], v[182:189], v[198:205], v[98:113], v169, v169 op_sel_hi:[0,0,0]
	v_mfma_scale_f32_32x32x64_f8f6f4 v[66:81], v[182:189], v[214:221], v[66:81], v169, v169 op_sel_hi:[0,0,0]
	v_mfma_scale_f32_32x32x64_f8f6f4 v[98:113], v[190:197], v[206:213], v[98:113], v169, v169 op_sel_hi:[0,0,0]
	v_mfma_scale_f32_32x32x64_f8f6f4 v[66:81], v[190:197], v[222:229], v[66:81], v169, v169 op_sel_hi:[0,0,0]
	s_setprio 0
	s_barrier
	s_add_i32 s65, s59, s50
	v_lshl_add_u64 v[154:155], s[44:45], 0, v[140:141]
	s_mov_b32 m0, s65
	ds_read_b128 v[198:201], v167 offset:16384
	ds_read_b128 v[206:209], v167 offset:17408
	ds_read_b128 v[202:205], v168 offset:16384
	ds_read_b128 v[210:213], v168 offset:17408
	ds_read_b128 v[214:217], v167 offset:20480
	ds_read_b128 v[222:225], v167 offset:21504
	ds_read_b128 v[218:221], v168 offset:20480
	ds_read_b128 v[226:229], v168 offset:21504
	global_load_lds_dwordx4 v[154:155], off
	s_add_i32 m0, s65, 0x2000
	s_add_u32 s66, s44, 0x40000
	v_lshl_add_u64 v[156:157], s[44:45], 0, v[144:145]
	s_addc_u32 s67, s45, 0
	s_add_i32 s65, s60, s50
	global_load_lds_dwordx4 v[156:157], off
	v_lshl_add_u64 v[230:231], s[66:67], 0, v[140:141]
	s_mov_b32 m0, s65
	v_lshl_add_u64 v[232:233], s[46:47], 0, v[142:143]
	global_load_lds_dwordx4 v[230:231], off
	v_lshl_add_u64 v[230:231], s[66:67], 0, v[144:145]
	s_add_i32 m0, s65, 0x2000
	s_nop 0
	global_load_lds_dwordx4 v[230:231], off
	s_waitcnt vmcnt(6)
	s_waitcnt lgkmcnt(0)
	s_barrier
	s_setprio 1
	v_mfma_scale_f32_32x32x64_f8f6f4 v[50:65], v[130:137], v[198:205], v[50:65], v169, v169 op_sel_hi:[0,0,0]
	v_mfma_scale_f32_32x32x64_f8f6f4 v[18:33], v[130:137], v[214:221], v[18:33], v169, v169 op_sel_hi:[0,0,0]
	v_mfma_scale_f32_32x32x64_f8f6f4 v[50:65], v[174:181], v[206:213], v[50:65], v169, v169 op_sel_hi:[0,0,0]
	v_lshl_add_u64 v[230:231], s[46:47], 0, v[138:139]
	s_mov_b32 m0, s51
	s_nop 0
	global_load_lds_dwordx4 v[230:231], off
	v_mfma_scale_f32_32x32x64_f8f6f4 v[18:33], v[174:181], v[222:229], v[18:33], v169, v169 op_sel_hi:[0,0,0]
	s_setprio 0
	s_setprio 1
	v_mfma_scale_f32_32x32x64_f8f6f4 v[34:49], v[182:189], v[198:205], v[34:49], v169, v169 op_sel_hi:[0,0,0]
	v_mfma_scale_f32_32x32x64_f8f6f4 v[2:17], v[182:189], v[214:221], v[2:17], v169, v169 op_sel_hi:[0,0,0]
	s_mov_b32 m0, s52
	s_nop 0
	global_load_lds_dwordx4 v[232:233], off
	v_mfma_scale_f32_32x32x64_f8f6f4 v[34:49], v[190:197], v[206:213], v[34:49], v169, v169 op_sel_hi:[0,0,0]
	v_mfma_scale_f32_32x32x64_f8f6f4 v[2:17], v[190:197], v[222:229], v[2:17], v169, v169 op_sel_hi:[0,0,0]
	s_setprio 0
	s_barrier
	s_add_i32 s65, 0, 0x18000
	s_add_i32 s66, 0, 0x1c000
	v_add_u32_e32 v130, s65, v1
	v_add_u32_e32 v134, s65, v158
	v_add_u32_e32 v182, s66, v1
	v_add_u32_e32 v186, s66, v158
	ds_read_b128 v[130:133], v130
	ds_read_b128 v[134:137], v134
	ds_read_b128 v[174:177], v170
	ds_read_b128 v[178:181], v171
	ds_read_b128 v[182:185], v182
	ds_read_b128 v[186:189], v186
	ds_read_b128 v[190:193], v172
	ds_read_b128 v[194:197], v173
	s_add_u32 s46, s46, 0x40000
	s_addc_u32 s47, s47, 0
	s_mov_b32 m0, s53
	v_lshl_add_u64 v[234:235], s[46:47], 0, v[138:139]
	ds_read_b128 v[198:201], v167 offset:32768
	ds_read_b128 v[206:209], v167 offset:33792
	ds_read_b128 v[202:205], v168 offset:32768
	ds_read_b128 v[210:213], v168 offset:33792
	ds_read_b128 v[214:217], v167 offset:36864
	ds_read_b128 v[222:225], v167 offset:37888
	ds_read_b128 v[218:221], v168 offset:36864
	ds_read_b128 v[226:229], v168 offset:37888
	global_load_lds_dwordx4 v[234:235], off
	v_lshl_add_u64 v[234:235], s[46:47], 0, v[142:143]
	s_mov_b32 m0, s54
	s_nop 0
	global_load_lds_dwordx4 v[234:235], off
	s_waitcnt vmcnt(8)
	s_waitcnt lgkmcnt(0)
	s_barrier
	s_setprio 1
	v_mfma_scale_f32_32x32x64_f8f6f4 v[114:129], v[130:137], v[198:205], v[114:129], v169, v169 op_sel_hi:[0,0,0]
	v_mfma_scale_f32_32x32x64_f8f6f4 v[82:97], v[130:137], v[214:221], v[82:97], v169, v169 op_sel_hi:[0,0,0]
	v_mfma_scale_f32_32x32x64_f8f6f4 v[114:129], v[174:181], v[206:213], v[114:129], v169, v169 op_sel_hi:[0,0,0]
	v_mfma_scale_f32_32x32x64_f8f6f4 v[82:97], v[174:181], v[222:229], v[82:97], v169, v169 op_sel_hi:[0,0,0]
	s_setprio 0
	s_setprio 1
	v_mfma_scale_f32_32x32x64_f8f6f4 v[98:113], v[182:189], v[198:205], v[98:113], v169, v169 op_sel_hi:[0,0,0]
	v_mfma_scale_f32_32x32x64_f8f6f4 v[66:81], v[182:189], v[214:221], v[66:81], v169, v169 op_sel_hi:[0,0,0]
	v_mfma_scale_f32_32x32x64_f8f6f4 v[98:113], v[190:197], v[206:213], v[98:113], v169, v169 op_sel_hi:[0,0,0]
	v_mfma_scale_f32_32x32x64_f8f6f4 v[66:81], v[190:197], v[222:229], v[66:81], v169, v169 op_sel_hi:[0,0,0]
	s_setprio 0
	s_barrier
	s_add_i32 s46, s65, s50
	v_lshl_add_u64 v[154:155], v[154:155], 0, s[14:15]
	s_mov_b32 m0, s46
	ds_read_b128 v[198:201], v167 offset:49152
	ds_read_b128 v[206:209], v167 offset:50176
	ds_read_b128 v[202:205], v168 offset:49152
	ds_read_b128 v[210:213], v168 offset:50176
	ds_read_b128 v[214:217], v167 offset:53248
	ds_read_b128 v[222:225], v167 offset:54272
	ds_read_b128 v[218:221], v168 offset:53248
	ds_read_b128 v[226:229], v168 offset:54272
	global_load_lds_dwordx4 v[154:155], off
	s_add_i32 m0, s46, 0x2000
	s_add_u32 s44, s44, 0x40080
	v_lshl_add_u64 v[154:155], v[156:157], 0, s[14:15]
	s_addc_u32 s45, s45, 0
	s_add_i32 s46, s66, s50
	global_load_lds_dwordx4 v[154:155], off
	v_lshl_add_u64 v[154:155], s[44:45], 0, v[140:141]
	s_mov_b32 m0, s46
	s_nop 0
	global_load_lds_dwordx4 v[154:155], off
	v_lshl_add_u64 v[154:155], s[44:45], 0, v[144:145]
	s_add_i32 m0, s46, 0x2000
	s_nop 0
	global_load_lds_dwordx4 v[154:155], off
	s_waitcnt vmcnt(6)
	s_waitcnt lgkmcnt(0)
	s_barrier
	s_setprio 1
	v_mfma_scale_f32_32x32x64_f8f6f4 v[50:65], v[130:137], v[198:205], v[50:65], v169, v169 op_sel_hi:[0,0,0]
	v_mfma_scale_f32_32x32x64_f8f6f4 v[18:33], v[130:137], v[214:221], v[18:33], v169, v169 op_sel_hi:[0,0,0]
	v_mfma_scale_f32_32x32x64_f8f6f4 v[50:65], v[174:181], v[206:213], v[50:65], v169, v169 op_sel_hi:[0,0,0]
	v_lshl_add_u64 v[154:155], v[230:231], 0, s[14:15]
	s_mov_b32 m0, s56
	s_nop 0
	global_load_lds_dwordx4 v[154:155], off
	v_mfma_scale_f32_32x32x64_f8f6f4 v[18:33], v[174:181], v[222:229], v[18:33], v169, v169 op_sel_hi:[0,0,0]
	s_setprio 0
	s_setprio 1
	v_mfma_scale_f32_32x32x64_f8f6f4 v[34:49], v[182:189], v[198:205], v[34:49], v169, v169 op_sel_hi:[0,0,0]
	v_mfma_scale_f32_32x32x64_f8f6f4 v[2:17], v[182:189], v[214:221], v[2:17], v169, v169 op_sel_hi:[0,0,0]
	v_lshl_add_u64 v[154:155], v[232:233], 0, s[14:15]
	s_mov_b32 m0, s57
	s_nop 0
	global_load_lds_dwordx4 v[154:155], off
	v_mfma_scale_f32_32x32x64_f8f6f4 v[34:49], v[190:197], v[206:213], v[34:49], v169, v169 op_sel_hi:[0,0,0]
	v_mfma_scale_f32_32x32x64_f8f6f4 v[2:17], v[190:197], v[222:229], v[2:17], v169, v169 op_sel_hi:[0,0,0]
	s_setprio 0
	s_barrier
	s_add_i32 s41, s41, 2
	s_add_u32 s42, s42, 0x100
	s_addc_u32 s43, s43, 0
	s_add_u32 s31, s31, 0x100
	s_addc_u32 s35, s35, 0
	s_cmp_gt_u32 s41, 13
	s_cbranch_scc0 .LBB0_769
	s_and_b64 vcc, exec, s[16:17]
	s_cbranch_vccz .LBB0_772
	s_barrier

.LBB0_925:
	s_waitcnt vmcnt(8)
	s_add_u32 s36, s30, 0x80
	s_waitcnt lgkmcnt(0)
	s_addc_u32 s37, s31, 0
	s_and_b64 s[34:35], s[34:35], exec
	v_mov_b32_e32 v205, v199
	s_cselect_b32 s37, s11, s37
	s_cselect_b32 s36, s10, s36
	s_cselect_b32 s35, s23, s27
	s_cselect_b32 s34, s22, s25
	s_barrier
	s_setprio 1
	v_mfma_scale_f32_32x32x64_f8f6f4 v[114:129], v[154:161], v[178:185], v[114:129], v224, v224 op_sel_hi:[0,0,0]
	v_mfma_scale_f32_32x32x64_f8f6f4 v[82:97], v[154:161], v[186:193], v[82:97], v224, v224 op_sel_hi:[0,0,0]
	v_mfma_scale_f32_32x32x64_f8f6f4 v[114:129], v[146:153], v[162:169], v[114:129], v224, v224 op_sel_hi:[0,0,0]
	v_mfma_scale_f32_32x32x64_f8f6f4 v[82:97], v[146:153], v[170:177], v[82:97], v224, v224 op_sel_hi:[0,0,0]
	s_setprio 0
	s_setprio 1
	v_mfma_scale_f32_32x32x64_f8f6f4 v[98:113], v[138:145], v[178:185], v[98:113], v224, v224 op_sel_hi:[0,0,0]
	v_mfma_scale_f32_32x32x64_f8f6f4 v[66:81], v[138:145], v[186:193], v[66:81], v224, v224 op_sel_hi:[0,0,0]
	v_mfma_scale_f32_32x32x64_f8f6f4 v[98:113], v[130:137], v[162:169], v[98:113], v224, v224 op_sel_hi:[0,0,0]
	v_mfma_scale_f32_32x32x64_f8f6f4 v[66:81], v[130:137], v[170:177], v[66:81], v224, v224 op_sel_hi:[0,0,0]
	s_setprio 0
	s_barrier
	s_mov_b32 m0, s42
	v_lshl_add_u64 v[232:233], s[34:35], 0, v[194:195]
	s_add_u32 s66, s34, 0x40000
	ds_read_b128 v[162:165], v221 offset:16384
	ds_read_b128 v[170:173], v221 offset:17408
	ds_read_b128 v[166:169], v223 offset:16384
	ds_read_b128 v[174:177], v223 offset:17408
	ds_read_b128 v[178:181], v221 offset:20480
	ds_read_b128 v[186:189], v221 offset:21504
	ds_read_b128 v[182:185], v223 offset:20480
	ds_read_b128 v[190:193], v223 offset:21504
	global_load_lds_dwordx4 v[232:233], off
	v_lshl_add_u64 v[234:235], s[34:35], 0, v[196:197]
	s_mov_b32 m0, s43
	s_addc_u32 s67, s35, 0
	global_load_lds_dwordx4 v[234:235], off
	v_lshl_add_u64 v[236:237], s[66:67], 0, v[194:195]
	s_mov_b32 m0, s44
	v_mov_b32_e32 v203, v199
	global_load_lds_dwordx4 v[236:237], off
	v_lshl_add_u64 v[236:237], s[66:67], 0, v[196:197]
	s_mov_b32 m0, s45
	v_lshl_add_u64 v[238:239], s[36:37], 0, v[202:203]
	global_load_lds_dwordx4 v[236:237], off
	s_waitcnt vmcnt(6)
	s_waitcnt lgkmcnt(0)
	s_barrier
	s_setprio 1
	v_mfma_scale_f32_32x32x64_f8f6f4 v[50:65], v[154:161], v[162:169], v[50:65], v224, v224 op_sel_hi:[0,0,0]
	v_mfma_scale_f32_32x32x64_f8f6f4 v[18:33], v[154:161], v[178:185], v[18:33], v224, v224 op_sel_hi:[0,0,0]
	v_mfma_scale_f32_32x32x64_f8f6f4 v[50:65], v[146:153], v[170:177], v[50:65], v224, v224 op_sel_hi:[0,0,0]
	s_mov_b32 m0, s41
	v_lshl_add_u64 v[236:237], s[36:37], 0, v[198:199]
	global_load_lds_dwordx4 v198, s[36:37]
	v_mfma_scale_f32_32x32x64_f8f6f4 v[18:33], v[146:153], v[186:193], v[18:33], v224, v224 op_sel_hi:[0,0,0]
	s_setprio 0
	s_setprio 1
	v_mfma_scale_f32_32x32x64_f8f6f4 v[34:49], v[138:145], v[162:169], v[34:49], v224, v224 op_sel_hi:[0,0,0]
	v_mfma_scale_f32_32x32x64_f8f6f4 v[2:17], v[138:145], v[178:185], v[2:17], v224, v224 op_sel_hi:[0,0,0]
	s_mov_b32 m0, s46
	s_nop 0
	global_load_lds_dwordx4 v202, s[36:37]
	v_mfma_scale_f32_32x32x64_f8f6f4 v[34:49], v[130:137], v[170:177], v[34:49], v224, v224 op_sel_hi:[0,0,0]
	v_mfma_scale_f32_32x32x64_f8f6f4 v[2:17], v[130:137], v[186:193], v[2:17], v224, v224 op_sel_hi:[0,0,0]
	s_setprio 0
	s_barrier
	s_add_i32 s65, 0, 0x18000
	s_add_i32 s66, 0, 0x1c000
	v_add_u32_e32 v130, s65, v210
	v_add_u32_e32 v134, s65, v211
	v_add_u32_e32 v138, s57, v210
	v_add_u32_e32 v142, s57, v211
	v_add_u32_e32 v146, s66, v210
	v_add_u32_e32 v150, s66, v211
	v_add_u32_e32 v154, s58, v210
	v_add_u32_e32 v158, s58, v211
	ds_read_b128 v[130:133], v130
	ds_read_b128 v[134:137], v134
	ds_read_b128 v[138:141], v138
	ds_read_b128 v[142:145], v142
	ds_read_b128 v[146:149], v146
	ds_read_b128 v[150:153], v150
	ds_read_b128 v[154:157], v154
	ds_read_b128 v[158:161], v158
	s_mov_b32 m0, s47
	v_lshl_add_u64 v[240:241], s[36:37], 0, v[200:201]
	ds_read_b128 v[162:165], v221 offset:32768
	ds_read_b128 v[170:173], v221 offset:33792
	ds_read_b128 v[166:169], v223 offset:32768
	ds_read_b128 v[174:177], v223 offset:33792
	ds_read_b128 v[178:181], v221 offset:36864
	ds_read_b128 v[186:189], v221 offset:37888
	ds_read_b128 v[182:185], v223 offset:36864
	ds_read_b128 v[190:193], v223 offset:37888
	global_load_lds_dwordx4 v[240:241], off
	v_lshl_add_u64 v[240:241], s[36:37], 0, v[204:205]
	s_mov_b32 m0, s48
	s_nop 0
	global_load_lds_dwordx4 v[240:241], off
	s_waitcnt vmcnt(8)
	s_waitcnt lgkmcnt(0)
	s_barrier
	s_setprio 1
	v_mfma_scale_f32_32x32x64_f8f6f4 v[114:129], v[130:137], v[162:169], v[114:129], v224, v224 op_sel_hi:[0,0,0]
	v_mfma_scale_f32_32x32x64_f8f6f4 v[82:97], v[130:137], v[178:185], v[82:97], v224, v224 op_sel_hi:[0,0,0]
	v_mfma_scale_f32_32x32x64_f8f6f4 v[114:129], v[138:145], v[170:177], v[114:129], v224, v224 op_sel_hi:[0,0,0]
	v_mfma_scale_f32_32x32x64_f8f6f4 v[82:97], v[138:145], v[186:193], v[82:97], v224, v224 op_sel_hi:[0,0,0]
	s_setprio 0
	s_setprio 1
	v_mfma_scale_f32_32x32x64_f8f6f4 v[98:113], v[146:153], v[162:169], v[98:113], v224, v224 op_sel_hi:[0,0,0]
	v_mfma_scale_f32_32x32x64_f8f6f4 v[66:81], v[146:153], v[178:185], v[66:81], v224, v224 op_sel_hi:[0,0,0]
	v_mfma_scale_f32_32x32x64_f8f6f4 v[98:113], v[154:161], v[170:177], v[98:113], v224, v224 op_sel_hi:[0,0,0]
	v_mfma_scale_f32_32x32x64_f8f6f4 v[66:81], v[154:161], v[186:193], v[66:81], v224, v224 op_sel_hi:[0,0,0]
	s_setprio 0
	s_barrier
	s_add_i32 s36, s65, s40
	v_lshl_add_u64 v[232:233], v[232:233], 0, s[14:15]
	s_mov_b32 m0, s36
	ds_read_b128 v[162:165], v221 offset:49152
	ds_read_b128 v[170:173], v221 offset:50176
	ds_read_b128 v[166:169], v223 offset:49152
	ds_read_b128 v[174:177], v223 offset:50176
	ds_read_b128 v[178:181], v221 offset:53248
	ds_read_b128 v[186:189], v221 offset:54272
	ds_read_b128 v[182:185], v223 offset:53248
	ds_read_b128 v[190:193], v223 offset:54272
	global_load_lds_dwordx4 v[232:233], off
	s_add_i32 m0, s36, 0x2000
	s_add_u32 s34, s34, 0x40080
	v_lshl_add_u64 v[232:233], v[234:235], 0, s[14:15]
	s_addc_u32 s35, s35, 0
	s_add_i32 s36, s66, s40
	global_load_lds_dwordx4 v[232:233], off
	v_lshl_add_u64 v[232:233], s[34:35], 0, v[194:195]
	s_mov_b32 m0, s36
	s_nop 0
	global_load_lds_dwordx4 v[232:233], off
	v_lshl_add_u64 v[232:233], s[34:35], 0, v[196:197]
	s_add_i32 m0, s36, 0x2000
	s_nop 0
	global_load_lds_dwordx4 v[232:233], off
	s_waitcnt vmcnt(6)
	s_waitcnt lgkmcnt(0)
	s_barrier
	s_setprio 1
	v_mfma_scale_f32_32x32x64_f8f6f4 v[50:65], v[130:137], v[162:169], v[50:65], v224, v224 op_sel_hi:[0,0,0]
	v_mfma_scale_f32_32x32x64_f8f6f4 v[18:33], v[130:137], v[178:185], v[18:33], v224, v224 op_sel_hi:[0,0,0]
	v_mfma_scale_f32_32x32x64_f8f6f4 v[50:65], v[138:145], v[170:177], v[50:65], v224, v224 op_sel_hi:[0,0,0]
	v_lshl_add_u64 v[232:233], v[236:237], 0, s[14:15]
	s_mov_b32 m0, s52
	s_nop 0
	global_load_lds_dwordx4 v[232:233], off
	v_mfma_scale_f32_32x32x64_f8f6f4 v[18:33], v[138:145], v[186:193], v[18:33], v224, v224 op_sel_hi:[0,0,0]
	s_setprio 0
	s_setprio 1
	v_mfma_scale_f32_32x32x64_f8f6f4 v[34:49], v[146:153], v[162:169], v[34:49], v224, v224 op_sel_hi:[0,0,0]
	v_mfma_scale_f32_32x32x64_f8f6f4 v[2:17], v[146:153], v[178:185], v[2:17], v224, v224 op_sel_hi:[0,0,0]
	v_lshl_add_u64 v[232:233], v[238:239], 0, s[14:15]
	s_mov_b32 m0, s53
	s_nop 0
	global_load_lds_dwordx4 v[232:233], off
	v_mfma_scale_f32_32x32x64_f8f6f4 v[34:49], v[154:161], v[170:177], v[34:49], v224, v224 op_sel_hi:[0,0,0]
	v_mfma_scale_f32_32x32x64_f8f6f4 v[2:17], v[154:161], v[186:193], v[2:17], v224, v224 op_sel_hi:[0,0,0]
	s_setprio 0
	s_barrier
	s_add_i32 s64, s64, 2
	s_add_u32 s30, s30, 0x100
	s_addc_u32 s31, s31, 0
	s_add_u32 s25, s25, 0x100
	s_addc_u32 s27, s27, 0
	s_cmp_gt_u32 s64, 13
	s_cbranch_scc1 .LBB0_928

.LBB0_1014:
	ds_read_b128 v[168:171], v150
	ds_read_b128 v[172:175], v151
	ds_read_b128 v[176:179], v152
	ds_read_b128 v[180:183], v153
	ds_read_b128 v[184:187], v154
	ds_read_b128 v[188:191], v155
	ds_read_b128 v[192:195], v156
	ds_read_b128 v[196:199], v157
	s_add_u32 s30, s28, 0xfffe0080
	s_addc_u32 s31, s29, -1
	s_cmp_eq_u32 s58, 4
	s_cselect_b32 s35, s21, s31
	s_cselect_b32 s34, s20, s30
	s_cselect_b32 s31, s23, s27
	s_cselect_b32 s30, s22, s25
	v_lshl_add_u64 v[144:145], s[28:29], 0, v[140:141]
	s_add_i32 m0, s37, 0xc000
	ds_read_b128 v[200:203], v158
	ds_read_b128 v[208:211], v158 offset:1024
	ds_read_b128 v[204:207], v159
	ds_read_b128 v[212:215], v159 offset:1024
	ds_read_b128 v[216:219], v158 offset:4096
	ds_read_b128 v[224:227], v158 offset:5120
	ds_read_b128 v[220:223], v159 offset:4096
	ds_read_b128 v[228:231], v159 offset:5120
	global_load_lds_dwordx4 v[144:145], off
	v_lshl_add_u64 v[144:145], s[28:29], 0, v[142:143]
	s_add_i32 m0, s37, 0xe000
	s_nop 0
	global_load_lds_dwordx4 v[144:145], off
	s_waitcnt vmcnt(8)
	s_waitcnt lgkmcnt(0)
	s_barrier
	s_setprio 1
	v_mfma_scale_f32_32x32x64_f8f6f4 v[114:129], v[168:175], v[200:207], v[114:129], v160, v160 op_sel_hi:[0,0,0]
	v_mfma_scale_f32_32x32x64_f8f6f4 v[82:97], v[168:175], v[216:223], v[82:97], v160, v160 op_sel_hi:[0,0,0]
	v_mfma_scale_f32_32x32x64_f8f6f4 v[114:129], v[176:183], v[208:215], v[114:129], v160, v160 op_sel_hi:[0,0,0]
	v_mfma_scale_f32_32x32x64_f8f6f4 v[82:97], v[176:183], v[224:231], v[82:97], v160, v160 op_sel_hi:[0,0,0]
	s_setprio 0
	s_setprio 1
	v_mfma_scale_f32_32x32x64_f8f6f4 v[98:113], v[184:191], v[200:207], v[98:113], v160, v160 op_sel_hi:[0,0,0]
	v_mfma_scale_f32_32x32x64_f8f6f4 v[66:81], v[184:191], v[216:223], v[66:81], v160, v160 op_sel_hi:[0,0,0]
	v_mfma_scale_f32_32x32x64_f8f6f4 v[98:113], v[192:199], v[208:215], v[98:113], v160, v160 op_sel_hi:[0,0,0]
	v_mfma_scale_f32_32x32x64_f8f6f4 v[66:81], v[192:199], v[224:231], v[66:81], v160, v160 op_sel_hi:[0,0,0]
	s_setprio 0
	s_barrier
	s_add_i32 s59, s51, s36
	v_lshl_add_u64 v[144:145], s[30:31], 0, v[132:133]
	s_mov_b32 m0, s59
	ds_read_b128 v[200:203], v158 offset:16384
	ds_read_b128 v[208:211], v158 offset:17408
	ds_read_b128 v[204:207], v159 offset:16384
	ds_read_b128 v[212:215], v159 offset:17408
	ds_read_b128 v[216:219], v158 offset:20480
	ds_read_b128 v[224:227], v158 offset:21504
	ds_read_b128 v[220:223], v159 offset:20480
	ds_read_b128 v[228:231], v159 offset:21504
	global_load_lds_dwordx4 v[144:145], off
	s_add_i32 m0, s59, 0x2000
	s_add_u32 s60, s30, 0x20000
	v_lshl_add_u64 v[146:147], s[30:31], 0, v[136:137]
	s_addc_u32 s61, s31, 0
	s_add_i32 s59, s52, s36
	global_load_lds_dwordx4 v[146:147], off
	v_lshl_add_u64 v[232:233], s[60:61], 0, v[132:133]
	s_mov_b32 m0, s59
	v_lshl_add_u64 v[234:235], s[34:35], 0, v[134:135]
	global_load_lds_dwordx4 v[232:233], off
	v_lshl_add_u64 v[232:233], s[60:61], 0, v[136:137]
	s_add_i32 m0, s59, 0x2000
	s_nop 0
	global_load_lds_dwordx4 v[232:233], off
	s_waitcnt vmcnt(6)
	s_waitcnt lgkmcnt(0)
	s_barrier
	s_setprio 1
	v_mfma_scale_f32_32x32x64_f8f6f4 v[50:65], v[168:175], v[200:207], v[50:65], v160, v160 op_sel_hi:[0,0,0]
	v_mfma_scale_f32_32x32x64_f8f6f4 v[18:33], v[168:175], v[216:223], v[18:33], v160, v160 op_sel_hi:[0,0,0]
	v_mfma_scale_f32_32x32x64_f8f6f4 v[50:65], v[176:183], v[208:215], v[50:65], v160, v160 op_sel_hi:[0,0,0]
	v_lshl_add_u64 v[232:233], s[34:35], 0, v[130:131]
	s_mov_b32 m0, s37
	s_nop 0
	global_load_lds_dwordx4 v[232:233], off
	v_mfma_scale_f32_32x32x64_f8f6f4 v[18:33], v[176:183], v[224:231], v[18:33], v160, v160 op_sel_hi:[0,0,0]
	s_setprio 0
	s_setprio 1
	v_mfma_scale_f32_32x32x64_f8f6f4 v[34:49], v[184:191], v[200:207], v[34:49], v160, v160 op_sel_hi:[0,0,0]
	v_mfma_scale_f32_32x32x64_f8f6f4 v[2:17], v[184:191], v[216:223], v[2:17], v160, v160 op_sel_hi:[0,0,0]
	s_mov_b32 m0, s38
	s_nop 0
	global_load_lds_dwordx4 v[234:235], off
	v_mfma_scale_f32_32x32x64_f8f6f4 v[34:49], v[192:199], v[208:215], v[34:49], v160, v160 op_sel_hi:[0,0,0]
	v_mfma_scale_f32_32x32x64_f8f6f4 v[2:17], v[192:199], v[224:231], v[2:17], v160, v160 op_sel_hi:[0,0,0]
	s_setprio 0
	s_barrier
	s_add_i32 s59, 0, 0x18000
	v_add_u32_e32 v167, s59, v1
	v_add_u32_e32 v172, s59, v148
	s_add_i32 s60, 0, 0x1c000
	ds_read_b128 v[168:171], v167
	ds_read_b128 v[172:175], v172
	ds_read_b128 v[176:179], v161
	ds_read_b128 v[180:183], v162
	v_add_u32_e32 v167, s60, v1
	v_add_u32_e32 v188, s60, v148
	ds_read_b128 v[184:187], v167
	ds_read_b128 v[188:191], v188
	ds_read_b128 v[192:195], v163
	ds_read_b128 v[196:199], v164
	s_add_u32 s34, s34, 0x20000
	s_addc_u32 s35, s35, 0
	s_mov_b32 m0, s39
	v_lshl_add_u64 v[236:237], s[34:35], 0, v[130:131]
	ds_read_b128 v[200:203], v158 offset:32768
	ds_read_b128 v[208:211], v158 offset:33792
	ds_read_b128 v[204:207], v159 offset:32768
	ds_read_b128 v[212:215], v159 offset:33792
	ds_read_b128 v[216:219], v158 offset:36864
	ds_read_b128 v[224:227], v158 offset:37888
	ds_read_b128 v[220:223], v159 offset:36864
	ds_read_b128 v[228:231], v159 offset:37888
	global_load_lds_dwordx4 v[236:237], off
	v_lshl_add_u64 v[236:237], s[34:35], 0, v[134:135]
	s_mov_b32 m0, s40
	s_nop 0
	global_load_lds_dwordx4 v[236:237], off
	s_waitcnt vmcnt(8)
	s_waitcnt lgkmcnt(0)
	s_barrier
	s_setprio 1
	v_mfma_scale_f32_32x32x64_f8f6f4 v[114:129], v[168:175], v[200:207], v[114:129], v160, v160 op_sel_hi:[0,0,0]
	v_mfma_scale_f32_32x32x64_f8f6f4 v[82:97], v[168:175], v[216:223], v[82:97], v160, v160 op_sel_hi:[0,0,0]
	v_mfma_scale_f32_32x32x64_f8f6f4 v[114:129], v[176:183], v[208:215], v[114:129], v160, v160 op_sel_hi:[0,0,0]
	v_mfma_scale_f32_32x32x64_f8f6f4 v[82:97], v[176:183], v[224:231], v[82:97], v160, v160 op_sel_hi:[0,0,0]
	s_setprio 0
	s_setprio 1
	v_mfma_scale_f32_32x32x64_f8f6f4 v[98:113], v[184:191], v[200:207], v[98:113], v160, v160 op_sel_hi:[0,0,0]
	v_mfma_scale_f32_32x32x64_f8f6f4 v[66:81], v[184:191], v[216:223], v[66:81], v160, v160 op_sel_hi:[0,0,0]
	v_mfma_scale_f32_32x32x64_f8f6f4 v[98:113], v[192:199], v[208:215], v[98:113], v160, v160 op_sel_hi:[0,0,0]
	v_mfma_scale_f32_32x32x64_f8f6f4 v[66:81], v[192:199], v[224:231], v[66:81], v160, v160 op_sel_hi:[0,0,0]
	s_setprio 0
	s_barrier
	s_add_i32 s34, s59, s36
	v_lshl_add_u64 v[144:145], v[144:145], 0, s[12:13]
	s_mov_b32 m0, s34
	ds_read_b128 v[200:203], v158 offset:49152
	ds_read_b128 v[208:211], v158 offset:50176
	ds_read_b128 v[204:207], v159 offset:49152
	ds_read_b128 v[212:215], v159 offset:50176
	ds_read_b128 v[216:219], v158 offset:53248
	ds_read_b128 v[224:227], v158 offset:54272
	ds_read_b128 v[220:223], v159 offset:53248
	ds_read_b128 v[228:231], v159 offset:54272
	global_load_lds_dwordx4 v[144:145], off
	s_add_i32 m0, s34, 0x2000
	s_add_u32 s30, s30, 0x20080
	v_lshl_add_u64 v[144:145], v[146:147], 0, s[12:13]
	s_addc_u32 s31, s31, 0
	s_add_i32 s34, s60, s36
	global_load_lds_dwordx4 v[144:145], off
	v_lshl_add_u64 v[144:145], s[30:31], 0, v[132:133]
	s_mov_b32 m0, s34
	s_nop 0
	global_load_lds_dwordx4 v[144:145], off
	v_lshl_add_u64 v[144:145], s[30:31], 0, v[136:137]
	s_add_i32 m0, s34, 0x2000
	s_nop 0
	global_load_lds_dwordx4 v[144:145], off
	s_waitcnt vmcnt(6)
	s_waitcnt lgkmcnt(0)
	s_barrier
	s_setprio 1
	v_mfma_scale_f32_32x32x64_f8f6f4 v[50:65], v[168:175], v[200:207], v[50:65], v160, v160 op_sel_hi:[0,0,0]
	v_mfma_scale_f32_32x32x64_f8f6f4 v[18:33], v[168:175], v[216:223], v[18:33], v160, v160 op_sel_hi:[0,0,0]
	v_mfma_scale_f32_32x32x64_f8f6f4 v[50:65], v[176:183], v[208:215], v[50:65], v160, v160 op_sel_hi:[0,0,0]
	v_lshl_add_u64 v[144:145], v[232:233], 0, s[12:13]
	s_mov_b32 m0, s46
	s_nop 0
	global_load_lds_dwordx4 v[144:145], off
	v_mfma_scale_f32_32x32x64_f8f6f4 v[18:33], v[176:183], v[224:231], v[18:33], v160, v160 op_sel_hi:[0,0,0]
	s_setprio 0
	s_setprio 1
	v_mfma_scale_f32_32x32x64_f8f6f4 v[34:49], v[184:191], v[200:207], v[34:49], v160, v160 op_sel_hi:[0,0,0]
	v_mfma_scale_f32_32x32x64_f8f6f4 v[2:17], v[184:191], v[216:223], v[2:17], v160, v160 op_sel_hi:[0,0,0]
	v_lshl_add_u64 v[144:145], v[234:235], 0, s[12:13]
	s_mov_b32 m0, s47
	s_nop 0
	global_load_lds_dwordx4 v[144:145], off
	v_mfma_scale_f32_32x32x64_f8f6f4 v[34:49], v[192:199], v[208:215], v[34:49], v160, v160 op_sel_hi:[0,0,0]
	v_mfma_scale_f32_32x32x64_f8f6f4 v[2:17], v[192:199], v[224:231], v[2:17], v160, v160 op_sel_hi:[0,0,0]
	s_setprio 0
	s_barrier
	s_add_i32 s58, s58, 2
	s_add_u32 s28, s28, 0x100
	s_addc_u32 s29, s29, 0
	s_add_u32 s25, s25, 0x100
	s_addc_u32 s27, s27, 0
	s_cmp_gt_u32 s58, 5
	s_cbranch_scc0 .LBB0_1014
	s_and_b64 vcc, exec, s[14:15]
	s_cbranch_vccz .LBB0_1017
	s_barrier

.LBB0_1147:
	v_add_u32_e32 v130, s63, v1
	v_add_u32_e32 v134, s63, v177
	v_add_u32_e32 v146, s64, v1
	v_add_u32_e32 v150, s64, v177
	ds_read_b128 v[130:133], v130
	ds_read_b128 v[134:137], v134
	ds_read_b128 v[138:141], v179
	ds_read_b128 v[142:145], v181
	ds_read_b128 v[146:149], v146
	ds_read_b128 v[150:153], v150
	ds_read_b128 v[154:157], v183
	ds_read_b128 v[158:161], v190
	s_add_u32 s42, s40, 0xfffc0080
	s_addc_u32 s43, s41, -1
	s_cmp_eq_u32 s35, 12
	s_cselect_b32 s45, s37, s43
	s_cselect_b32 s44, s36, s42
	s_cselect_b32 s43, s39, s31
	s_cselect_b32 s42, s38, s7
	v_lshl_add_u64 v[184:185], s[40:41], 0, v[172:173]
	s_add_i32 m0, s51, 0xc000
	ds_read_b128 v[208:211], v191
	ds_read_b128 v[216:219], v191 offset:1024
	ds_read_b128 v[212:215], v192
	ds_read_b128 v[220:223], v192 offset:1024
	ds_read_b128 v[224:227], v191 offset:4096
	ds_read_b128 v[232:235], v191 offset:5120
	ds_read_b128 v[228:231], v192 offset:4096
	ds_read_b128 v[236:239], v192 offset:5120
	global_load_lds_dwordx4 v[184:185], off
	v_lshl_add_u64 v[184:185], s[40:41], 0, v[174:175]
	s_add_i32 m0, s51, 0xe000
	s_nop 0
	global_load_lds_dwordx4 v[184:185], off
	s_waitcnt vmcnt(8)
	s_waitcnt lgkmcnt(0)
	s_barrier
	s_setprio 1
	v_mfma_scale_f32_32x32x64_f8f6f4 v[114:129], v[130:137], v[208:215], v[114:129], v193, v193 op_sel_hi:[0,0,0]
	v_mfma_scale_f32_32x32x64_f8f6f4 v[82:97], v[130:137], v[224:231], v[82:97], v193, v193 op_sel_hi:[0,0,0]
	v_mfma_scale_f32_32x32x64_f8f6f4 v[114:129], v[138:145], v[216:223], v[114:129], v193, v193 op_sel_hi:[0,0,0]
	v_mfma_scale_f32_32x32x64_f8f6f4 v[82:97], v[138:145], v[232:239], v[82:97], v193, v193 op_sel_hi:[0,0,0]
	s_setprio 0
	s_setprio 1
	v_mfma_scale_f32_32x32x64_f8f6f4 v[98:113], v[146:153], v[208:215], v[98:113], v193, v193 op_sel_hi:[0,0,0]
	v_mfma_scale_f32_32x32x64_f8f6f4 v[66:81], v[146:153], v[224:231], v[66:81], v193, v193 op_sel_hi:[0,0,0]
	v_mfma_scale_f32_32x32x64_f8f6f4 v[98:113], v[154:161], v[216:223], v[98:113], v193, v193 op_sel_hi:[0,0,0]
	v_mfma_scale_f32_32x32x64_f8f6f4 v[66:81], v[154:161], v[232:239], v[66:81], v193, v193 op_sel_hi:[0,0,0]
	s_setprio 0
	s_barrier
	s_add_i32 s46, s63, s50
	v_lshl_add_u64 v[184:185], s[42:43], 0, v[164:165]
	s_mov_b32 m0, s46
	ds_read_b128 v[208:211], v191 offset:16384
	ds_read_b128 v[216:219], v191 offset:17408
	ds_read_b128 v[212:215], v192 offset:16384
	ds_read_b128 v[220:223], v192 offset:17408
	ds_read_b128 v[224:227], v191 offset:20480
	ds_read_b128 v[232:235], v191 offset:21504
	ds_read_b128 v[228:231], v192 offset:20480
	ds_read_b128 v[236:239], v192 offset:21504
	global_load_lds_dwordx4 v[184:185], off
	s_add_i32 m0, s46, 0x2000
	s_add_u32 s46, s42, 0x40000
	v_lshl_add_u64 v[186:187], s[42:43], 0, v[168:169]
	s_addc_u32 s47, s43, 0
	s_add_i32 s70, s64, s50
	global_load_lds_dwordx4 v[186:187], off
	v_lshl_add_u64 v[188:189], s[46:47], 0, v[164:165]
	s_mov_b32 m0, s70
	v_lshl_add_u64 v[240:241], s[44:45], 0, v[166:167]
	global_load_lds_dwordx4 v[188:189], off
	v_lshl_add_u64 v[188:189], s[46:47], 0, v[168:169]
	s_add_i32 m0, s70, 0x2000
	s_nop 0
	global_load_lds_dwordx4 v[188:189], off
	s_waitcnt vmcnt(6)
	s_waitcnt lgkmcnt(0)
	s_barrier
	s_setprio 1
	v_mfma_scale_f32_32x32x64_f8f6f4 v[50:65], v[130:137], v[208:215], v[50:65], v193, v193 op_sel_hi:[0,0,0]
	v_mfma_scale_f32_32x32x64_f8f6f4 v[18:33], v[130:137], v[224:231], v[18:33], v193, v193 op_sel_hi:[0,0,0]
	v_mfma_scale_f32_32x32x64_f8f6f4 v[50:65], v[138:145], v[216:223], v[50:65], v193, v193 op_sel_hi:[0,0,0]
	v_lshl_add_u64 v[188:189], s[44:45], 0, v[162:163]
	s_mov_b32 m0, s51
	s_nop 0
	global_load_lds_dwordx4 v[188:189], off
	v_mfma_scale_f32_32x32x64_f8f6f4 v[18:33], v[138:145], v[232:239], v[18:33], v193, v193 op_sel_hi:[0,0,0]
	s_setprio 0
	s_setprio 1
	v_mfma_scale_f32_32x32x64_f8f6f4 v[34:49], v[146:153], v[208:215], v[34:49], v193, v193 op_sel_hi:[0,0,0]
	v_mfma_scale_f32_32x32x64_f8f6f4 v[2:17], v[146:153], v[224:231], v[2:17], v193, v193 op_sel_hi:[0,0,0]
	s_mov_b32 m0, s52
	s_nop 0
	global_load_lds_dwordx4 v[240:241], off
	v_mfma_scale_f32_32x32x64_f8f6f4 v[34:49], v[154:161], v[216:223], v[34:49], v193, v193 op_sel_hi:[0,0,0]
	v_mfma_scale_f32_32x32x64_f8f6f4 v[2:17], v[154:161], v[232:239], v[2:17], v193, v193 op_sel_hi:[0,0,0]
	s_setprio 0
	s_barrier
	s_add_i32 s46, 0, 0x18000
	s_add_i32 s47, 0, 0x1c000
	v_add_u32_e32 v130, s46, v1
	v_add_u32_e32 v134, s46, v177
	v_add_u32_e32 v146, s47, v1
	v_add_u32_e32 v150, s47, v177
	ds_read_b128 v[130:133], v130
	ds_read_b128 v[134:137], v134
	ds_read_b128 v[138:141], v194
	ds_read_b128 v[142:145], v195
	ds_read_b128 v[146:149], v146
	ds_read_b128 v[150:153], v150
	ds_read_b128 v[154:157], v196
	ds_read_b128 v[158:161], v197
	s_add_u32 s44, s44, 0x40000
	s_addc_u32 s45, s45, 0
	s_mov_b32 m0, s53
	v_lshl_add_u64 v[242:243], s[44:45], 0, v[162:163]
	ds_read_b128 v[208:211], v191 offset:32768
	ds_read_b128 v[216:219], v191 offset:33792
	ds_read_b128 v[212:215], v192 offset:32768
	ds_read_b128 v[220:223], v192 offset:33792
	ds_read_b128 v[224:227], v191 offset:36864
	ds_read_b128 v[232:235], v191 offset:37888
	ds_read_b128 v[228:231], v192 offset:36864
	ds_read_b128 v[236:239], v192 offset:37888
	global_load_lds_dwordx4 v[242:243], off
	v_lshl_add_u64 v[242:243], s[44:45], 0, v[166:167]
	s_mov_b32 m0, s54
	s_nop 0
	global_load_lds_dwordx4 v[242:243], off
	s_waitcnt vmcnt(8)
	s_waitcnt lgkmcnt(0)
	s_barrier
	s_setprio 1
	v_mfma_scale_f32_32x32x64_f8f6f4 v[114:129], v[130:137], v[208:215], v[114:129], v193, v193 op_sel_hi:[0,0,0]
	v_mfma_scale_f32_32x32x64_f8f6f4 v[82:97], v[130:137], v[224:231], v[82:97], v193, v193 op_sel_hi:[0,0,0]
	v_mfma_scale_f32_32x32x64_f8f6f4 v[114:129], v[138:145], v[216:223], v[114:129], v193, v193 op_sel_hi:[0,0,0]
	v_mfma_scale_f32_32x32x64_f8f6f4 v[82:97], v[138:145], v[232:239], v[82:97], v193, v193 op_sel_hi:[0,0,0]
	s_setprio 0
	s_setprio 1
	v_mfma_scale_f32_32x32x64_f8f6f4 v[98:113], v[146:153], v[208:215], v[98:113], v193, v193 op_sel_hi:[0,0,0]
	v_mfma_scale_f32_32x32x64_f8f6f4 v[66:81], v[146:153], v[224:231], v[66:81], v193, v193 op_sel_hi:[0,0,0]
	v_mfma_scale_f32_32x32x64_f8f6f4 v[98:113], v[154:161], v[216:223], v[98:113], v193, v193 op_sel_hi:[0,0,0]
	v_mfma_scale_f32_32x32x64_f8f6f4 v[66:81], v[154:161], v[232:239], v[66:81], v193, v193 op_sel_hi:[0,0,0]
	s_setprio 0
	s_barrier
	s_add_i32 s44, s46, s50
	v_lshl_add_u64 v[184:185], v[184:185], 0, s[20:21]
	s_mov_b32 m0, s44
	ds_read_b128 v[208:211], v191 offset:49152
	ds_read_b128 v[216:219], v191 offset:50176
	ds_read_b128 v[212:215], v192 offset:49152
	ds_read_b128 v[220:223], v192 offset:50176
	ds_read_b128 v[224:227], v191 offset:53248
	ds_read_b128 v[232:235], v191 offset:54272
	ds_read_b128 v[228:231], v192 offset:53248
	ds_read_b128 v[236:239], v192 offset:54272
	global_load_lds_dwordx4 v[184:185], off
	s_add_i32 m0, s44, 0x2000
	s_add_u32 s42, s42, 0x40080
	v_lshl_add_u64 v[184:185], v[186:187], 0, s[20:21]
	s_addc_u32 s43, s43, 0
	s_add_i32 s44, s47, s50
	global_load_lds_dwordx4 v[184:185], off
	v_lshl_add_u64 v[184:185], s[42:43], 0, v[164:165]
	s_mov_b32 m0, s44
	s_nop 0
	global_load_lds_dwordx4 v[184:185], off
	v_lshl_add_u64 v[184:185], s[42:43], 0, v[168:169]
	s_add_i32 m0, s44, 0x2000
	s_nop 0
	global_load_lds_dwordx4 v[184:185], off
	s_waitcnt vmcnt(6)
	s_waitcnt lgkmcnt(0)
	s_barrier
	s_setprio 1
	v_mfma_scale_f32_32x32x64_f8f6f4 v[50:65], v[130:137], v[208:215], v[50:65], v193, v193 op_sel_hi:[0,0,0]
	v_mfma_scale_f32_32x32x64_f8f6f4 v[18:33], v[130:137], v[224:231], v[18:33], v193, v193 op_sel_hi:[0,0,0]
	v_mfma_scale_f32_32x32x64_f8f6f4 v[50:65], v[138:145], v[216:223], v[50:65], v193, v193 op_sel_hi:[0,0,0]
	v_lshl_add_u64 v[184:185], v[188:189], 0, s[20:21]
	s_mov_b32 m0, s57
	s_nop 0
	global_load_lds_dwordx4 v[184:185], off
	v_mfma_scale_f32_32x32x64_f8f6f4 v[18:33], v[138:145], v[232:239], v[18:33], v193, v193 op_sel_hi:[0,0,0]
	s_setprio 0
	s_setprio 1
	v_mfma_scale_f32_32x32x64_f8f6f4 v[34:49], v[146:153], v[208:215], v[34:49], v193, v193 op_sel_hi:[0,0,0]
	v_mfma_scale_f32_32x32x64_f8f6f4 v[2:17], v[146:153], v[224:231], v[2:17], v193, v193 op_sel_hi:[0,0,0]
	v_lshl_add_u64 v[184:185], v[240:241], 0, s[20:21]
	s_mov_b32 m0, s58
	s_nop 0
	global_load_lds_dwordx4 v[184:185], off
	v_mfma_scale_f32_32x32x64_f8f6f4 v[34:49], v[154:161], v[216:223], v[34:49], v193, v193 op_sel_hi:[0,0,0]
	v_mfma_scale_f32_32x32x64_f8f6f4 v[2:17], v[154:161], v[232:239], v[2:17], v193, v193 op_sel_hi:[0,0,0]
	s_setprio 0
	s_barrier
	s_add_i32 s35, s35, 2
	s_add_u32 s40, s40, 0x100
	s_addc_u32 s41, s41, 0
	s_add_u32 s7, s7, 0x100
	s_addc_u32 s31, s31, 0
	s_cmp_gt_u32 s35, 13
	s_cbranch_scc0 .LBB0_1147
	s_and_b64 vcc, exec, s[22:23]
	s_cbranch_vccz .LBB0_1150
	s_barrier

.LBB0_1536:
	s_waitcnt vmcnt(8)
	s_add_u32 s34, s28, 0x80
	s_waitcnt lgkmcnt(0)
	s_addc_u32 s35, s29, 0
	s_and_b64 s[30:31], s[30:31], exec
	v_mov_b32_e32 v205, v199
	s_cselect_b32 s35, s9, s35
	s_cselect_b32 s34, s8, s34
	s_cselect_b32 s31, s21, s25
	s_cselect_b32 s30, s20, s23
	s_barrier
	s_setprio 1
	v_mfma_scale_f32_32x32x64_f8f6f4 v[114:129], v[154:161], v[178:185], v[114:129], v224, v224 op_sel_hi:[0,0,0]
	v_mfma_scale_f32_32x32x64_f8f6f4 v[82:97], v[154:161], v[186:193], v[82:97], v224, v224 op_sel_hi:[0,0,0]
	v_mfma_scale_f32_32x32x64_f8f6f4 v[114:129], v[146:153], v[162:169], v[114:129], v224, v224 op_sel_hi:[0,0,0]
	v_mfma_scale_f32_32x32x64_f8f6f4 v[82:97], v[146:153], v[170:177], v[82:97], v224, v224 op_sel_hi:[0,0,0]
	s_setprio 0
	s_setprio 1
	v_mfma_scale_f32_32x32x64_f8f6f4 v[98:113], v[138:145], v[178:185], v[98:113], v224, v224 op_sel_hi:[0,0,0]
	v_mfma_scale_f32_32x32x64_f8f6f4 v[66:81], v[138:145], v[186:193], v[66:81], v224, v224 op_sel_hi:[0,0,0]
	v_mfma_scale_f32_32x32x64_f8f6f4 v[98:113], v[130:137], v[162:169], v[98:113], v224, v224 op_sel_hi:[0,0,0]
	v_mfma_scale_f32_32x32x64_f8f6f4 v[66:81], v[130:137], v[170:177], v[66:81], v224, v224 op_sel_hi:[0,0,0]
	s_setprio 0
	s_barrier
	s_mov_b32 m0, s40
	v_lshl_add_u64 v[232:233], s[30:31], 0, v[194:195]
	s_add_u32 s64, s30, 0x40000
	ds_read_b128 v[162:165], v221 offset:16384
	ds_read_b128 v[170:173], v221 offset:17408
	ds_read_b128 v[166:169], v223 offset:16384
	ds_read_b128 v[174:177], v223 offset:17408
	ds_read_b128 v[178:181], v221 offset:20480
	ds_read_b128 v[186:189], v221 offset:21504
	ds_read_b128 v[182:185], v223 offset:20480
	ds_read_b128 v[190:193], v223 offset:21504
	global_load_lds_dwordx4 v[232:233], off
	v_lshl_add_u64 v[234:235], s[30:31], 0, v[196:197]
	s_mov_b32 m0, s41
	s_addc_u32 s65, s31, 0
	global_load_lds_dwordx4 v[234:235], off
	v_lshl_add_u64 v[236:237], s[64:65], 0, v[194:195]
	s_mov_b32 m0, s42
	v_mov_b32_e32 v203, v199
	global_load_lds_dwordx4 v[236:237], off
	v_lshl_add_u64 v[236:237], s[64:65], 0, v[196:197]
	s_mov_b32 m0, s43
	v_lshl_add_u64 v[238:239], s[34:35], 0, v[202:203]
	global_load_lds_dwordx4 v[236:237], off
	s_waitcnt vmcnt(6)
	s_waitcnt lgkmcnt(0)
	s_barrier
	s_setprio 1
	v_mfma_scale_f32_32x32x64_f8f6f4 v[50:65], v[154:161], v[162:169], v[50:65], v224, v224 op_sel_hi:[0,0,0]
	v_mfma_scale_f32_32x32x64_f8f6f4 v[18:33], v[154:161], v[178:185], v[18:33], v224, v224 op_sel_hi:[0,0,0]
	v_mfma_scale_f32_32x32x64_f8f6f4 v[50:65], v[146:153], v[170:177], v[50:65], v224, v224 op_sel_hi:[0,0,0]
	s_mov_b32 m0, s39
	v_lshl_add_u64 v[236:237], s[34:35], 0, v[198:199]
	global_load_lds_dwordx4 v198, s[34:35]
	v_mfma_scale_f32_32x32x64_f8f6f4 v[18:33], v[146:153], v[186:193], v[18:33], v224, v224 op_sel_hi:[0,0,0]
	s_setprio 0
	s_setprio 1
	v_mfma_scale_f32_32x32x64_f8f6f4 v[34:49], v[138:145], v[162:169], v[34:49], v224, v224 op_sel_hi:[0,0,0]
	v_mfma_scale_f32_32x32x64_f8f6f4 v[2:17], v[138:145], v[178:185], v[2:17], v224, v224 op_sel_hi:[0,0,0]
	s_mov_b32 m0, s44
	s_nop 0
	global_load_lds_dwordx4 v202, s[34:35]
	v_mfma_scale_f32_32x32x64_f8f6f4 v[34:49], v[130:137], v[170:177], v[34:49], v224, v224 op_sel_hi:[0,0,0]
	v_mfma_scale_f32_32x32x64_f8f6f4 v[2:17], v[130:137], v[186:193], v[2:17], v224, v224 op_sel_hi:[0,0,0]
	s_setprio 0
	s_barrier
	s_add_i32 s63, 0, 0x18000
	s_add_i32 s64, 0, 0x1c000
	v_add_u32_e32 v130, s63, v210
	v_add_u32_e32 v134, s63, v211
	v_add_u32_e32 v138, s55, v210
	v_add_u32_e32 v142, s55, v211
	v_add_u32_e32 v146, s64, v210
	v_add_u32_e32 v150, s64, v211
	v_add_u32_e32 v154, s56, v210
	v_add_u32_e32 v158, s56, v211
	ds_read_b128 v[130:133], v130
	ds_read_b128 v[134:137], v134
	ds_read_b128 v[138:141], v138
	ds_read_b128 v[142:145], v142
	ds_read_b128 v[146:149], v146
	ds_read_b128 v[150:153], v150
	ds_read_b128 v[154:157], v154
	ds_read_b128 v[158:161], v158
	s_mov_b32 m0, s45
	v_lshl_add_u64 v[240:241], s[34:35], 0, v[200:201]
	ds_read_b128 v[162:165], v221 offset:32768
	ds_read_b128 v[170:173], v221 offset:33792
	ds_read_b128 v[166:169], v223 offset:32768
	ds_read_b128 v[174:177], v223 offset:33792
	ds_read_b128 v[178:181], v221 offset:36864
	ds_read_b128 v[186:189], v221 offset:37888
	ds_read_b128 v[182:185], v223 offset:36864
	ds_read_b128 v[190:193], v223 offset:37888
	global_load_lds_dwordx4 v[240:241], off
	v_lshl_add_u64 v[240:241], s[34:35], 0, v[204:205]
	s_mov_b32 m0, s46
	s_nop 0
	global_load_lds_dwordx4 v[240:241], off
	s_waitcnt vmcnt(8)
	s_waitcnt lgkmcnt(0)
	s_barrier
	s_setprio 1
	v_mfma_scale_f32_32x32x64_f8f6f4 v[114:129], v[130:137], v[162:169], v[114:129], v224, v224 op_sel_hi:[0,0,0]
	v_mfma_scale_f32_32x32x64_f8f6f4 v[82:97], v[130:137], v[178:185], v[82:97], v224, v224 op_sel_hi:[0,0,0]
	v_mfma_scale_f32_32x32x64_f8f6f4 v[114:129], v[138:145], v[170:177], v[114:129], v224, v224 op_sel_hi:[0,0,0]
	v_mfma_scale_f32_32x32x64_f8f6f4 v[82:97], v[138:145], v[186:193], v[82:97], v224, v224 op_sel_hi:[0,0,0]
	s_setprio 0
	s_setprio 1
	v_mfma_scale_f32_32x32x64_f8f6f4 v[98:113], v[146:153], v[162:169], v[98:113], v224, v224 op_sel_hi:[0,0,0]
	v_mfma_scale_f32_32x32x64_f8f6f4 v[66:81], v[146:153], v[178:185], v[66:81], v224, v224 op_sel_hi:[0,0,0]
	v_mfma_scale_f32_32x32x64_f8f6f4 v[98:113], v[154:161], v[170:177], v[98:113], v224, v224 op_sel_hi:[0,0,0]
	v_mfma_scale_f32_32x32x64_f8f6f4 v[66:81], v[154:161], v[186:193], v[66:81], v224, v224 op_sel_hi:[0,0,0]
	s_setprio 0
	s_barrier
	s_add_i32 s34, s63, s38
	v_lshl_add_u64 v[232:233], v[232:233], 0, s[12:13]
	s_mov_b32 m0, s34
	ds_read_b128 v[162:165], v221 offset:49152
	ds_read_b128 v[170:173], v221 offset:50176
	ds_read_b128 v[166:169], v223 offset:49152
	ds_read_b128 v[174:177], v223 offset:50176
	ds_read_b128 v[178:181], v221 offset:53248
	ds_read_b128 v[186:189], v221 offset:54272
	ds_read_b128 v[182:185], v223 offset:53248
	ds_read_b128 v[190:193], v223 offset:54272
	global_load_lds_dwordx4 v[232:233], off
	s_add_i32 m0, s34, 0x2000
	s_add_u32 s30, s30, 0x40080
	v_lshl_add_u64 v[232:233], v[234:235], 0, s[12:13]
	s_addc_u32 s31, s31, 0
	s_add_i32 s34, s64, s38
	global_load_lds_dwordx4 v[232:233], off
	v_lshl_add_u64 v[232:233], s[30:31], 0, v[194:195]
	s_mov_b32 m0, s34
	s_nop 0
	global_load_lds_dwordx4 v[232:233], off
	v_lshl_add_u64 v[232:233], s[30:31], 0, v[196:197]
	s_add_i32 m0, s34, 0x2000
	s_nop 0
	global_load_lds_dwordx4 v[232:233], off
	s_waitcnt vmcnt(6)
	s_waitcnt lgkmcnt(0)
	s_barrier
	s_setprio 1
	v_mfma_scale_f32_32x32x64_f8f6f4 v[50:65], v[130:137], v[162:169], v[50:65], v224, v224 op_sel_hi:[0,0,0]
	v_mfma_scale_f32_32x32x64_f8f6f4 v[18:33], v[130:137], v[178:185], v[18:33], v224, v224 op_sel_hi:[0,0,0]
	v_mfma_scale_f32_32x32x64_f8f6f4 v[50:65], v[138:145], v[170:177], v[50:65], v224, v224 op_sel_hi:[0,0,0]
	v_lshl_add_u64 v[232:233], v[236:237], 0, s[12:13]
	s_mov_b32 m0, s50
	s_nop 0
	global_load_lds_dwordx4 v[232:233], off
	v_mfma_scale_f32_32x32x64_f8f6f4 v[18:33], v[138:145], v[186:193], v[18:33], v224, v224 op_sel_hi:[0,0,0]
	s_setprio 0
	s_setprio 1
	v_mfma_scale_f32_32x32x64_f8f6f4 v[34:49], v[146:153], v[162:169], v[34:49], v224, v224 op_sel_hi:[0,0,0]
	v_mfma_scale_f32_32x32x64_f8f6f4 v[2:17], v[146:153], v[178:185], v[2:17], v224, v224 op_sel_hi:[0,0,0]
	v_lshl_add_u64 v[232:233], v[238:239], 0, s[12:13]
	s_mov_b32 m0, s51
	s_nop 0
	global_load_lds_dwordx4 v[232:233], off
	v_mfma_scale_f32_32x32x64_f8f6f4 v[34:49], v[154:161], v[170:177], v[34:49], v224, v224 op_sel_hi:[0,0,0]
	v_mfma_scale_f32_32x32x64_f8f6f4 v[2:17], v[154:161], v[186:193], v[2:17], v224, v224 op_sel_hi:[0,0,0]
	s_setprio 0
	s_barrier
	s_add_i32 s62, s62, 2
	s_add_u32 s28, s28, 0x100
	s_addc_u32 s29, s29, 0
	s_add_u32 s23, s23, 0x100
	s_addc_u32 s25, s25, 0
	s_cmp_gt_u32 s62, 13
	s_cbranch_scc1 .LBB0_1539

.LBB0_1625:
	ds_read_b128 v[168:171], v150
	ds_read_b128 v[172:175], v151
	ds_read_b128 v[176:179], v152
	ds_read_b128 v[180:183], v153
	ds_read_b128 v[184:187], v154
	ds_read_b128 v[188:191], v155
	ds_read_b128 v[192:195], v156
	ds_read_b128 v[196:199], v157
	s_add_u32 s28, s26, 0xfffe0080
	s_addc_u32 s29, s27, -1
	s_cmp_eq_u32 s56, 4
	s_cselect_b32 s31, s19, s29
	s_cselect_b32 s30, s18, s28
	s_cselect_b32 s29, s21, s25
	s_cselect_b32 s28, s20, s23
	v_lshl_add_u64 v[144:145], s[26:27], 0, v[140:141]
	s_add_i32 m0, s35, 0xc000
	ds_read_b128 v[200:203], v158
	ds_read_b128 v[208:211], v158 offset:1024
	ds_read_b128 v[204:207], v159
	ds_read_b128 v[212:215], v159 offset:1024
	ds_read_b128 v[216:219], v158 offset:4096
	ds_read_b128 v[224:227], v158 offset:5120
	ds_read_b128 v[220:223], v159 offset:4096
	ds_read_b128 v[228:231], v159 offset:5120
	global_load_lds_dwordx4 v[144:145], off
	v_lshl_add_u64 v[144:145], s[26:27], 0, v[142:143]
	s_add_i32 m0, s35, 0xe000
	s_nop 0
	global_load_lds_dwordx4 v[144:145], off
	s_waitcnt vmcnt(8)
	s_waitcnt lgkmcnt(0)
	s_barrier
	s_setprio 1
	v_mfma_scale_f32_32x32x64_f8f6f4 v[114:129], v[168:175], v[200:207], v[114:129], v160, v160 op_sel_hi:[0,0,0]
	v_mfma_scale_f32_32x32x64_f8f6f4 v[82:97], v[168:175], v[216:223], v[82:97], v160, v160 op_sel_hi:[0,0,0]
	v_mfma_scale_f32_32x32x64_f8f6f4 v[114:129], v[176:183], v[208:215], v[114:129], v160, v160 op_sel_hi:[0,0,0]
	v_mfma_scale_f32_32x32x64_f8f6f4 v[82:97], v[176:183], v[224:231], v[82:97], v160, v160 op_sel_hi:[0,0,0]
	s_setprio 0
	s_setprio 1
	v_mfma_scale_f32_32x32x64_f8f6f4 v[98:113], v[184:191], v[200:207], v[98:113], v160, v160 op_sel_hi:[0,0,0]
	v_mfma_scale_f32_32x32x64_f8f6f4 v[66:81], v[184:191], v[216:223], v[66:81], v160, v160 op_sel_hi:[0,0,0]
	v_mfma_scale_f32_32x32x64_f8f6f4 v[98:113], v[192:199], v[208:215], v[98:113], v160, v160 op_sel_hi:[0,0,0]
	v_mfma_scale_f32_32x32x64_f8f6f4 v[66:81], v[192:199], v[224:231], v[66:81], v160, v160 op_sel_hi:[0,0,0]
	s_setprio 0
	s_barrier
	s_add_i32 s57, s49, s34
	v_lshl_add_u64 v[144:145], s[28:29], 0, v[132:133]
	s_mov_b32 m0, s57
	ds_read_b128 v[200:203], v158 offset:16384
	ds_read_b128 v[208:211], v158 offset:17408
	ds_read_b128 v[204:207], v159 offset:16384
	ds_read_b128 v[212:215], v159 offset:17408
	ds_read_b128 v[216:219], v158 offset:20480
	ds_read_b128 v[224:227], v158 offset:21504
	ds_read_b128 v[220:223], v159 offset:20480
	ds_read_b128 v[228:231], v159 offset:21504
	global_load_lds_dwordx4 v[144:145], off
	s_add_i32 m0, s57, 0x2000
	s_add_u32 s58, s28, 0x20000
	v_lshl_add_u64 v[146:147], s[28:29], 0, v[136:137]
	s_addc_u32 s59, s29, 0
	s_add_i32 s57, s50, s34
	global_load_lds_dwordx4 v[146:147], off
	v_lshl_add_u64 v[232:233], s[58:59], 0, v[132:133]
	s_mov_b32 m0, s57
	v_lshl_add_u64 v[234:235], s[30:31], 0, v[134:135]
	global_load_lds_dwordx4 v[232:233], off
	v_lshl_add_u64 v[232:233], s[58:59], 0, v[136:137]
	s_add_i32 m0, s57, 0x2000
	s_nop 0
	global_load_lds_dwordx4 v[232:233], off
	s_waitcnt vmcnt(6)
	s_waitcnt lgkmcnt(0)
	s_barrier
	s_setprio 1
	v_mfma_scale_f32_32x32x64_f8f6f4 v[50:65], v[168:175], v[200:207], v[50:65], v160, v160 op_sel_hi:[0,0,0]
	v_mfma_scale_f32_32x32x64_f8f6f4 v[18:33], v[168:175], v[216:223], v[18:33], v160, v160 op_sel_hi:[0,0,0]
	v_mfma_scale_f32_32x32x64_f8f6f4 v[50:65], v[176:183], v[208:215], v[50:65], v160, v160 op_sel_hi:[0,0,0]
	v_lshl_add_u64 v[232:233], s[30:31], 0, v[130:131]
	s_mov_b32 m0, s35
	s_nop 0
	global_load_lds_dwordx4 v[232:233], off
	v_mfma_scale_f32_32x32x64_f8f6f4 v[18:33], v[176:183], v[224:231], v[18:33], v160, v160 op_sel_hi:[0,0,0]
	s_setprio 0
	s_setprio 1
	v_mfma_scale_f32_32x32x64_f8f6f4 v[34:49], v[184:191], v[200:207], v[34:49], v160, v160 op_sel_hi:[0,0,0]
	v_mfma_scale_f32_32x32x64_f8f6f4 v[2:17], v[184:191], v[216:223], v[2:17], v160, v160 op_sel_hi:[0,0,0]
	s_mov_b32 m0, s36
	s_nop 0
	global_load_lds_dwordx4 v[234:235], off
	v_mfma_scale_f32_32x32x64_f8f6f4 v[34:49], v[192:199], v[208:215], v[34:49], v160, v160 op_sel_hi:[0,0,0]
	v_mfma_scale_f32_32x32x64_f8f6f4 v[2:17], v[192:199], v[224:231], v[2:17], v160, v160 op_sel_hi:[0,0,0]
	s_setprio 0
	s_barrier
	s_add_i32 s57, 0, 0x18000
	v_add_u32_e32 v167, s57, v1
	v_add_u32_e32 v172, s57, v148
	s_add_i32 s58, 0, 0x1c000
	ds_read_b128 v[168:171], v167
	ds_read_b128 v[172:175], v172
	ds_read_b128 v[176:179], v161
	ds_read_b128 v[180:183], v162
	v_add_u32_e32 v167, s58, v1
	v_add_u32_e32 v188, s58, v148
	ds_read_b128 v[184:187], v167
	ds_read_b128 v[188:191], v188
	ds_read_b128 v[192:195], v163
	ds_read_b128 v[196:199], v164
	s_add_u32 s30, s30, 0x20000
	s_addc_u32 s31, s31, 0
	s_mov_b32 m0, s37
	v_lshl_add_u64 v[236:237], s[30:31], 0, v[130:131]
	ds_read_b128 v[200:203], v158 offset:32768
	ds_read_b128 v[208:211], v158 offset:33792
	ds_read_b128 v[204:207], v159 offset:32768
	ds_read_b128 v[212:215], v159 offset:33792
	ds_read_b128 v[216:219], v158 offset:36864
	ds_read_b128 v[224:227], v158 offset:37888
	ds_read_b128 v[220:223], v159 offset:36864
	ds_read_b128 v[228:231], v159 offset:37888
	global_load_lds_dwordx4 v[236:237], off
	v_lshl_add_u64 v[236:237], s[30:31], 0, v[134:135]
	s_mov_b32 m0, s38
	s_nop 0
	global_load_lds_dwordx4 v[236:237], off
	s_waitcnt vmcnt(8)
	s_waitcnt lgkmcnt(0)
	s_barrier
	s_setprio 1
	v_mfma_scale_f32_32x32x64_f8f6f4 v[114:129], v[168:175], v[200:207], v[114:129], v160, v160 op_sel_hi:[0,0,0]
	v_mfma_scale_f32_32x32x64_f8f6f4 v[82:97], v[168:175], v[216:223], v[82:97], v160, v160 op_sel_hi:[0,0,0]
	v_mfma_scale_f32_32x32x64_f8f6f4 v[114:129], v[176:183], v[208:215], v[114:129], v160, v160 op_sel_hi:[0,0,0]
	v_mfma_scale_f32_32x32x64_f8f6f4 v[82:97], v[176:183], v[224:231], v[82:97], v160, v160 op_sel_hi:[0,0,0]
	s_setprio 0
	s_setprio 1
	v_mfma_scale_f32_32x32x64_f8f6f4 v[98:113], v[184:191], v[200:207], v[98:113], v160, v160 op_sel_hi:[0,0,0]
	v_mfma_scale_f32_32x32x64_f8f6f4 v[66:81], v[184:191], v[216:223], v[66:81], v160, v160 op_sel_hi:[0,0,0]
	v_mfma_scale_f32_32x32x64_f8f6f4 v[98:113], v[192:199], v[208:215], v[98:113], v160, v160 op_sel_hi:[0,0,0]
	v_mfma_scale_f32_32x32x64_f8f6f4 v[66:81], v[192:199], v[224:231], v[66:81], v160, v160 op_sel_hi:[0,0,0]
	s_setprio 0
	s_barrier
	s_add_i32 s30, s57, s34
	v_lshl_add_u64 v[144:145], v[144:145], 0, s[10:11]
	s_mov_b32 m0, s30
	ds_read_b128 v[200:203], v158 offset:49152
	ds_read_b128 v[208:211], v158 offset:50176
	ds_read_b128 v[204:207], v159 offset:49152
	ds_read_b128 v[212:215], v159 offset:50176
	ds_read_b128 v[216:219], v158 offset:53248
	ds_read_b128 v[224:227], v158 offset:54272
	ds_read_b128 v[220:223], v159 offset:53248
	ds_read_b128 v[228:231], v159 offset:54272
	global_load_lds_dwordx4 v[144:145], off
	s_add_i32 m0, s30, 0x2000
	s_add_u32 s28, s28, 0x20080
	v_lshl_add_u64 v[144:145], v[146:147], 0, s[10:11]
	s_addc_u32 s29, s29, 0
	s_add_i32 s30, s58, s34
	global_load_lds_dwordx4 v[144:145], off
	v_lshl_add_u64 v[144:145], s[28:29], 0, v[132:133]
	s_mov_b32 m0, s30
	s_nop 0
	global_load_lds_dwordx4 v[144:145], off
	v_lshl_add_u64 v[144:145], s[28:29], 0, v[136:137]
	s_add_i32 m0, s30, 0x2000
	s_nop 0
	global_load_lds_dwordx4 v[144:145], off
	s_waitcnt vmcnt(6)
	s_waitcnt lgkmcnt(0)
	s_barrier
	s_setprio 1
	v_mfma_scale_f32_32x32x64_f8f6f4 v[50:65], v[168:175], v[200:207], v[50:65], v160, v160 op_sel_hi:[0,0,0]
	v_mfma_scale_f32_32x32x64_f8f6f4 v[18:33], v[168:175], v[216:223], v[18:33], v160, v160 op_sel_hi:[0,0,0]
	v_mfma_scale_f32_32x32x64_f8f6f4 v[50:65], v[176:183], v[208:215], v[50:65], v160, v160 op_sel_hi:[0,0,0]
	v_lshl_add_u64 v[144:145], v[232:233], 0, s[10:11]
	s_mov_b32 m0, s44
	s_nop 0
	global_load_lds_dwordx4 v[144:145], off
	v_mfma_scale_f32_32x32x64_f8f6f4 v[18:33], v[176:183], v[224:231], v[18:33], v160, v160 op_sel_hi:[0,0,0]
	s_setprio 0
	s_setprio 1
	v_mfma_scale_f32_32x32x64_f8f6f4 v[34:49], v[184:191], v[200:207], v[34:49], v160, v160 op_sel_hi:[0,0,0]
	v_mfma_scale_f32_32x32x64_f8f6f4 v[2:17], v[184:191], v[216:223], v[2:17], v160, v160 op_sel_hi:[0,0,0]
	v_lshl_add_u64 v[144:145], v[234:235], 0, s[10:11]
	s_mov_b32 m0, s45
	s_nop 0
	global_load_lds_dwordx4 v[144:145], off
	v_mfma_scale_f32_32x32x64_f8f6f4 v[34:49], v[192:199], v[208:215], v[34:49], v160, v160 op_sel_hi:[0,0,0]
	v_mfma_scale_f32_32x32x64_f8f6f4 v[2:17], v[192:199], v[224:231], v[2:17], v160, v160 op_sel_hi:[0,0,0]
	s_setprio 0
	s_barrier
	s_add_i32 s56, s56, 2
	s_add_u32 s26, s26, 0x100
	s_addc_u32 s27, s27, 0
	s_add_u32 s23, s23, 0x100
	s_addc_u32 s25, s25, 0
	s_cmp_gt_u32 s56, 5
	s_cbranch_scc0 .LBB0_1625
	s_and_b64 vcc, exec, s[12:13]
	s_cbranch_vccz .LBB0_1628
	s_barrier
